# best3 with chains ordered to share the B-fragment pair between consecutive chains
# speedup vs baseline: 1.0181x; 1.0035x over previous
; #define PG8_MMA(ai, bj, At, Bt) do { __builtin_amdgcn_s_setprio(1); _Pragma("unroll") for (int m = 0; m < 4; ++m) _Pragma("unroll") for (int n = 0; n < 2; ++n) _Pragma("unroll") for (int k = 0; k < 2; ++k) \
;         acc[ai][bj][m][n] = __builtin_amdgcn_mfma_f32_16x16x32_bf16(Bt[n][k], At[m][k], acc[ai][bj][m][n], 0, 0, 0); __builtin_amdgcn_s_setprio(0); } while (0)
; #define PG8_WAIT_V(n) asm volatile("s_waitcnt vmcnt(" #n ")" ::: "memory")
; #define PG8_TRIP_HEAD(T) const int t = (T); const bool last = (t == nt - 2); \
;             const char* a1 = cA + (size_t)(t + 1) * kstep; \
;             const char* a2 = last ? nA : cA + (size_t)(t + 2) * kstep; const char* b2 = last ? nB : cB + (size_t)(t + 2) * kstep; \
;             const char* a3 = a2 + kstep; const char* b3 = b2 + kstep; \
;             if (last && has_next) S.a_ready(nxt);
; template <class Epi, class Sched, bool ALIGN_EPI = false, bool SP2 = false>
; __device__ __forceinline__ void gemm_phase(PG8_LAS unsigned char* lds, const Gemm g, const Sched& S, const Epi& E) {
;     ...
;         if constexpr (SP2) {
;             { PG8_TRIP_HEAD(0) PG8_TRIP_SP2(asm volatile("s_waitcnt vmcnt(%0)" :: "n"(8 + Epi::NST) : "memory"), PG8_MMAZ) }
;             for (int tt = 2; tt < nt; tt += 2) { PG8_TRIP_HEAD(tt) PG8_TRIP_SP2(PG8_WAIT_V(8), PG8_MMA) }
.LBB0_130:
	ds_read_b128 v[144:147], v140
	ds_read_b128 v[148:151], v140 offset:1024
	ds_read_b128 v[152:155], v140 offset:2048
	ds_read_b128 v[156:159], v140 offset:3072
	ds_read_b128 v[164:167], v141
	ds_read_b128 v[168:171], v141 offset:1024
	ds_read_b128 v[172:175], v141 offset:2048
	ds_read_b128 v[176:179], v141 offset:3072
	s_add_u32 s31, s10, 0xfff7c080
	s_addc_u32 s53, s11, -1
	s_cmp_eq_u32 s30, 28
	s_cselect_b32 s55, s25, s53
	s_cselect_b32 s54, s24, s31
	s_cselect_b32 s57, s4, s29
	s_cselect_b32 s56, s5, s28
	s_mov_b32 m0, s23
	v_lshl_add_u64 v[184:185], s[10:11], 0, v[138:139]
	ds_read_b128 v[180:183], v163
	ds_read_b128 v[190:193], v163 offset:1024
	ds_read_b128 v[194:197], v163 offset:2048
	ds_read_b128 v[198:201], v163 offset:3072
	ds_read_b128 v[202:205], v163 offset:4096
	ds_read_b128 v[206:209], v163 offset:5120
	ds_read_b128 v[216:219], v163 offset:6144
	ds_read_b128 v[220:223], v163 offset:7168
	global_load_lds_dwordx4 v[184:185], off
	v_lshl_add_u64 v[184:185], v[184:185], 0, s[96:97]
	s_mov_b32 m0, s33
	s_nop 0
	global_load_lds_dwordx4 v[184:185], off
	s_waitcnt vmcnt(8)
	s_waitcnt lgkmcnt(0)
	s_barrier
	v_mfma_f32_16x16x32_bf16 v[120:123], v[144:147], v[180:183], v[120:123]
	v_mfma_f32_16x16x32_bf16 v[120:123], v[148:151], v[190:193], v[120:123]
	v_mfma_f32_16x16x32_bf16 v[104:107], v[144:147], v[194:197], v[104:107]
	v_mfma_f32_16x16x32_bf16 v[104:107], v[148:151], v[198:201], v[104:107]
	v_mfma_f32_16x16x32_bf16 v[88:91], v[144:147], v[202:205], v[88:91]
	v_mfma_f32_16x16x32_bf16 v[88:91], v[148:151], v[206:209], v[88:91]
	v_mfma_f32_16x16x32_bf16 v[72:75], v[144:147], v[216:219], v[72:75]
	v_mfma_f32_16x16x32_bf16 v[72:75], v[148:151], v[220:223], v[72:75]
	v_mfma_f32_16x16x32_bf16 v[116:119], v[152:155], v[180:183], v[116:119]
	v_mfma_f32_16x16x32_bf16 v[116:119], v[156:159], v[190:193], v[116:119]
	v_mfma_f32_16x16x32_bf16 v[100:103], v[152:155], v[194:197], v[100:103]
	v_mfma_f32_16x16x32_bf16 v[100:103], v[156:159], v[198:201], v[100:103]
	v_mfma_f32_16x16x32_bf16 v[84:87], v[152:155], v[202:205], v[84:87]
	v_mfma_f32_16x16x32_bf16 v[84:87], v[156:159], v[206:209], v[84:87]
	v_mfma_f32_16x16x32_bf16 v[68:71], v[152:155], v[216:219], v[68:71]
	v_mfma_f32_16x16x32_bf16 v[68:71], v[156:159], v[220:223], v[68:71]
	v_mfma_f32_16x16x32_bf16 v[128:131], v[164:167], v[180:183], v[128:131]
	v_mfma_f32_16x16x32_bf16 v[128:131], v[168:171], v[190:193], v[128:131]
	v_mfma_f32_16x16x32_bf16 v[112:115], v[164:167], v[194:197], v[112:115]
	v_mfma_f32_16x16x32_bf16 v[112:115], v[168:171], v[198:201], v[112:115]
	v_mfma_f32_16x16x32_bf16 v[96:99], v[164:167], v[202:205], v[96:99]
	v_mfma_f32_16x16x32_bf16 v[96:99], v[168:171], v[206:209], v[96:99]
	v_mfma_f32_16x16x32_bf16 v[80:83], v[164:167], v[216:219], v[80:83]
	v_mfma_f32_16x16x32_bf16 v[80:83], v[168:171], v[220:223], v[80:83]
	v_mfma_f32_16x16x32_bf16 v[124:127], v[172:175], v[180:183], v[124:127]
	v_mfma_f32_16x16x32_bf16 v[124:127], v[176:179], v[190:193], v[124:127]
	v_mfma_f32_16x16x32_bf16 v[108:111], v[172:175], v[194:197], v[108:111]
	v_mfma_f32_16x16x32_bf16 v[108:111], v[176:179], v[198:201], v[108:111]
	v_mfma_f32_16x16x32_bf16 v[92:95], v[172:175], v[202:205], v[92:95]
	v_mfma_f32_16x16x32_bf16 v[92:95], v[176:179], v[206:209], v[92:95]
	v_mfma_f32_16x16x32_bf16 v[76:79], v[172:175], v[216:219], v[76:79]
	v_mfma_f32_16x16x32_bf16 v[76:79], v[176:179], v[220:223], v[76:79]
	s_barrier
	s_mov_b32 m0, s45
	v_lshl_add_u64 v[184:185], s[56:57], 0, v[132:133]
	ds_read_b128 v[180:183], v163 offset:16384
	ds_read_b128 v[190:193], v163 offset:17408
	ds_read_b128 v[194:197], v163 offset:18432
	ds_read_b128 v[198:201], v163 offset:19456
	ds_read_b128 v[202:205], v163 offset:20480
	ds_read_b128 v[206:209], v163 offset:21504
	ds_read_b128 v[216:219], v163 offset:22528
	ds_read_b128 v[220:223], v163 offset:23552
	global_load_lds_dwordx4 v[184:185], off
	v_lshl_add_u64 v[186:187], v[184:185], 0, s[90:91]
	s_mov_b32 m0, s46
	s_nop 0
	global_load_lds_dwordx4 v[186:187], off
	v_lshl_add_u64 v[186:187], v[184:185], 0, s[60:61]
	s_mov_b32 m0, s47
	s_nop 0
	global_load_lds_dwordx4 v[186:187], off
	v_lshl_add_u64 v[186:187], v[184:185], 0, s[64:65]
	s_mov_b32 m0, s48
	s_nop 0
	global_load_lds_dwordx4 v[186:187], off
	v_lshl_add_u64 v[186:187], s[54:55], 0, v[134:135]
	s_mov_b32 m0, s37
	v_lshl_add_u64 v[188:189], v[186:187], 0, s[96:97]
	global_load_lds_dwordx4 v[186:187], off
	s_mov_b32 m0, s38
	s_nop 0
	global_load_lds_dwordx4 v[188:189], off
	s_waitcnt vmcnt(8)
	s_waitcnt lgkmcnt(0)
	s_barrier
	v_mfma_f32_16x16x32_bf16 v[56:59], v[144:147], v[180:183], v[56:59]
	v_mfma_f32_16x16x32_bf16 v[56:59], v[148:151], v[190:193], v[56:59]
	v_mfma_f32_16x16x32_bf16 v[40:43], v[144:147], v[194:197], v[40:43]
	v_mfma_f32_16x16x32_bf16 v[40:43], v[148:151], v[198:201], v[40:43]
	v_mfma_f32_16x16x32_bf16 v[24:27], v[144:147], v[202:205], v[24:27]
	v_mfma_f32_16x16x32_bf16 v[24:27], v[148:151], v[206:209], v[24:27]
	v_mfma_f32_16x16x32_bf16 v[8:11], v[144:147], v[216:219], v[8:11]
	v_mfma_f32_16x16x32_bf16 v[8:11], v[148:151], v[220:223], v[8:11]
	v_mfma_f32_16x16x32_bf16 v[52:55], v[152:155], v[180:183], v[52:55]
	v_mfma_f32_16x16x32_bf16 v[52:55], v[156:159], v[190:193], v[52:55]
	v_mfma_f32_16x16x32_bf16 v[36:39], v[152:155], v[194:197], v[36:39]
	v_mfma_f32_16x16x32_bf16 v[36:39], v[156:159], v[198:201], v[36:39]
	v_mfma_f32_16x16x32_bf16 v[20:23], v[152:155], v[202:205], v[20:23]
	v_mfma_f32_16x16x32_bf16 v[20:23], v[156:159], v[206:209], v[20:23]
	v_mfma_f32_16x16x32_bf16 v[4:7], v[152:155], v[216:219], v[4:7]
	v_mfma_f32_16x16x32_bf16 v[4:7], v[156:159], v[220:223], v[4:7]
	v_mfma_f32_16x16x32_bf16 v[64:67], v[164:167], v[180:183], v[64:67]
	v_mfma_f32_16x16x32_bf16 v[64:67], v[168:171], v[190:193], v[64:67]
	v_mfma_f32_16x16x32_bf16 v[48:51], v[164:167], v[194:197], v[48:51]
	v_mfma_f32_16x16x32_bf16 v[48:51], v[168:171], v[198:201], v[48:51]
	v_mfma_f32_16x16x32_bf16 v[32:35], v[164:167], v[202:205], v[32:35]
	v_mfma_f32_16x16x32_bf16 v[32:35], v[168:171], v[206:209], v[32:35]
	v_mfma_f32_16x16x32_bf16 v[16:19], v[164:167], v[216:219], v[16:19]
	v_mfma_f32_16x16x32_bf16 v[16:19], v[168:171], v[220:223], v[16:19]
	v_mfma_f32_16x16x32_bf16 v[60:63], v[172:175], v[180:183], v[60:63]
	v_mfma_f32_16x16x32_bf16 v[60:63], v[176:179], v[190:193], v[60:63]
	v_mfma_f32_16x16x32_bf16 v[44:47], v[172:175], v[194:197], v[44:47]
	v_mfma_f32_16x16x32_bf16 v[44:47], v[176:179], v[198:201], v[44:47]
	v_mfma_f32_16x16x32_bf16 v[28:31], v[172:175], v[202:205], v[28:31]
	v_mfma_f32_16x16x32_bf16 v[28:31], v[176:179], v[206:209], v[28:31]
	v_mfma_f32_16x16x32_bf16 v[12:15], v[172:175], v[216:219], v[12:15]
	v_mfma_f32_16x16x32_bf16 v[12:15], v[176:179], v[220:223], v[12:15]
	s_barrier
	ds_read_b128 v[144:147], v142
	ds_read_b128 v[148:151], v142 offset:1024
	ds_read_b128 v[152:155], v142 offset:2048
	ds_read_b128 v[156:159], v142 offset:3072
	ds_read_b128 v[164:167], v143
	ds_read_b128 v[168:171], v143 offset:1024
	ds_read_b128 v[172:175], v143 offset:2048
	ds_read_b128 v[176:179], v143 offset:3072
	s_mov_b32 m0, s39
	v_lshl_add_u64 v[188:189], v[186:187], 0, s[82:83]
	ds_read_b128 v[180:183], v163 offset:32768
	ds_read_b128 v[190:193], v163 offset:33792
	ds_read_b128 v[194:197], v163 offset:34816
	ds_read_b128 v[198:201], v163 offset:35840
	ds_read_b128 v[202:205], v163 offset:36864
	ds_read_b128 v[206:209], v163 offset:37888
	ds_read_b128 v[216:219], v163 offset:38912
	ds_read_b128 v[220:223], v163 offset:39936
	global_load_lds_dwordx4 v[188:189], off
	v_lshl_add_u64 v[188:189], v[186:187], 0, s[68:69]
	s_mov_b32 m0, s40
	s_nop 0
	global_load_lds_dwordx4 v[188:189], off
	s_waitcnt vmcnt(8)
	s_waitcnt lgkmcnt(0)
	s_barrier
	v_mfma_f32_16x16x32_bf16 v[120:123], v[144:147], v[180:183], v[120:123]
	v_mfma_f32_16x16x32_bf16 v[120:123], v[148:151], v[190:193], v[120:123]
	v_mfma_f32_16x16x32_bf16 v[104:107], v[144:147], v[194:197], v[104:107]
	v_mfma_f32_16x16x32_bf16 v[104:107], v[148:151], v[198:201], v[104:107]
	v_mfma_f32_16x16x32_bf16 v[88:91], v[144:147], v[202:205], v[88:91]
	v_mfma_f32_16x16x32_bf16 v[88:91], v[148:151], v[206:209], v[88:91]
	v_mfma_f32_16x16x32_bf16 v[72:75], v[144:147], v[216:219], v[72:75]
	v_mfma_f32_16x16x32_bf16 v[72:75], v[148:151], v[220:223], v[72:75]
	v_mfma_f32_16x16x32_bf16 v[116:119], v[152:155], v[180:183], v[116:119]
	v_mfma_f32_16x16x32_bf16 v[116:119], v[156:159], v[190:193], v[116:119]
	v_mfma_f32_16x16x32_bf16 v[100:103], v[152:155], v[194:197], v[100:103]
	v_mfma_f32_16x16x32_bf16 v[100:103], v[156:159], v[198:201], v[100:103]
	v_mfma_f32_16x16x32_bf16 v[84:87], v[152:155], v[202:205], v[84:87]
	v_mfma_f32_16x16x32_bf16 v[84:87], v[156:159], v[206:209], v[84:87]
	v_mfma_f32_16x16x32_bf16 v[68:71], v[152:155], v[216:219], v[68:71]
	v_mfma_f32_16x16x32_bf16 v[68:71], v[156:159], v[220:223], v[68:71]
	v_mfma_f32_16x16x32_bf16 v[128:131], v[164:167], v[180:183], v[128:131]
	v_mfma_f32_16x16x32_bf16 v[128:131], v[168:171], v[190:193], v[128:131]
	v_mfma_f32_16x16x32_bf16 v[112:115], v[164:167], v[194:197], v[112:115]
	v_mfma_f32_16x16x32_bf16 v[112:115], v[168:171], v[198:201], v[112:115]
	v_mfma_f32_16x16x32_bf16 v[96:99], v[164:167], v[202:205], v[96:99]
	v_mfma_f32_16x16x32_bf16 v[96:99], v[168:171], v[206:209], v[96:99]
	v_mfma_f32_16x16x32_bf16 v[80:83], v[164:167], v[216:219], v[80:83]
	v_mfma_f32_16x16x32_bf16 v[80:83], v[168:171], v[220:223], v[80:83]
	v_mfma_f32_16x16x32_bf16 v[124:127], v[172:175], v[180:183], v[124:127]
	v_mfma_f32_16x16x32_bf16 v[124:127], v[176:179], v[190:193], v[124:127]
	v_mfma_f32_16x16x32_bf16 v[108:111], v[172:175], v[194:197], v[108:111]
	v_mfma_f32_16x16x32_bf16 v[108:111], v[176:179], v[198:201], v[108:111]
	v_mfma_f32_16x16x32_bf16 v[92:95], v[172:175], v[202:205], v[92:95]
	v_mfma_f32_16x16x32_bf16 v[92:95], v[176:179], v[206:209], v[92:95]
	v_mfma_f32_16x16x32_bf16 v[76:79], v[172:175], v[216:219], v[76:79]
	v_mfma_f32_16x16x32_bf16 v[76:79], v[176:179], v[220:223], v[76:79]
	s_barrier
; #define PG8_MMA(ai, bj, At, Bt) do { __builtin_amdgcn_s_setprio(1); _Pragma("unroll") for (int m = 0; m < 4; ++m) _Pragma("unroll") for (int n = 0; n < 2; ++n) _Pragma("unroll") for (int k = 0; k < 2; ++k) \
;         acc[ai][bj][m][n] = __builtin_amdgcn_mfma_f32_16x16x32_bf16(Bt[n][k], At[m][k], acc[ai][bj][m][n], 0, 0, 0); __builtin_amdgcn_s_setprio(0); } while (0)
; #define PG8_WAIT_V(n) asm volatile("s_waitcnt vmcnt(" #n ")" ::: "memory")
; #define PG8_TRIP_HEAD(T) const int t = (T); const bool last = (t == nt - 2); \
;             const char* a1 = cA + (size_t)(t + 1) * kstep; \
;             const char* a2 = last ? nA : cA + (size_t)(t + 2) * kstep; const char* b2 = last ? nB : cB + (size_t)(t + 2) * kstep; \
;             const char* a3 = a2 + kstep; const char* b3 = b2 + kstep; \
;             if (last && has_next) S.a_ready(nxt);
; template <class Epi, class Sched, bool ALIGN_EPI = false, bool SP2 = false>
; __device__ __forceinline__ void gemm_phase(PG8_LAS unsigned char* lds, const Gemm g, const Sched& S, const Epi& E) {
;     ...
;         if constexpr (SP2) {
;             { PG8_TRIP_HEAD(0) PG8_TRIP_SP2(asm volatile("s_waitcnt vmcnt(%0)" :: "n"(8 + Epi::NST) : "memory"), PG8_MMAZ) }
;             for (int tt = 2; tt < nt; tt += 2) { PG8_TRIP_HEAD(tt) PG8_TRIP_SP2(PG8_WAIT_V(8), PG8_MMA) }
	s_mov_b32 m0, s49
	v_lshl_add_u64 v[188:189], v[184:185], 0, s[78:79]
	ds_read_b128 v[180:183], v163 offset:49152
	ds_read_b128 v[190:193], v163 offset:50176
	ds_read_b128 v[194:197], v163 offset:51200
	ds_read_b128 v[198:201], v163 offset:52224
	ds_read_b128 v[202:205], v163 offset:53248
	ds_read_b128 v[206:209], v163 offset:54272
	ds_read_b128 v[216:219], v163 offset:55296
	ds_read_b128 v[220:223], v163 offset:56320
	global_load_lds_dwordx4 v[188:189], off
	v_lshl_add_u64 v[188:189], v[184:185], 0, s[84:85]
	s_mov_b32 m0, s50
	s_nop 0
	global_load_lds_dwordx4 v[188:189], off
	v_lshl_add_u64 v[188:189], v[184:185], 0, s[62:63]
	s_mov_b32 m0, s51
	v_lshl_add_u64 v[184:185], v[184:185], 0, s[66:67]
	global_load_lds_dwordx4 v[188:189], off
	s_mov_b32 m0, s52
	s_nop 0
	global_load_lds_dwordx4 v[184:185], off
	v_lshl_add_u64 v[184:185], v[186:187], 0, s[78:79]
	s_mov_b32 m0, s0
	s_nop 0
	global_load_lds_dwordx4 v[184:185], off
	v_lshl_add_u64 v[184:185], v[186:187], 0, s[92:93]
	s_mov_b32 m0, s41
	s_nop 0
	global_load_lds_dwordx4 v[184:185], off
	s_waitcnt vmcnt(8)
	s_waitcnt lgkmcnt(0)
	s_barrier
	v_mfma_f32_16x16x32_bf16 v[56:59], v[144:147], v[180:183], v[56:59]
	v_mfma_f32_16x16x32_bf16 v[56:59], v[148:151], v[190:193], v[56:59]
	v_mfma_f32_16x16x32_bf16 v[40:43], v[144:147], v[194:197], v[40:43]
	v_mfma_f32_16x16x32_bf16 v[40:43], v[148:151], v[198:201], v[40:43]
	v_mfma_f32_16x16x32_bf16 v[24:27], v[144:147], v[202:205], v[24:27]
	v_mfma_f32_16x16x32_bf16 v[24:27], v[148:151], v[206:209], v[24:27]
	v_mfma_f32_16x16x32_bf16 v[8:11], v[144:147], v[216:219], v[8:11]
	v_mfma_f32_16x16x32_bf16 v[8:11], v[148:151], v[220:223], v[8:11]
	v_mfma_f32_16x16x32_bf16 v[52:55], v[152:155], v[180:183], v[52:55]
	v_mfma_f32_16x16x32_bf16 v[52:55], v[156:159], v[190:193], v[52:55]
	v_mfma_f32_16x16x32_bf16 v[36:39], v[152:155], v[194:197], v[36:39]
	v_mfma_f32_16x16x32_bf16 v[36:39], v[156:159], v[198:201], v[36:39]
	v_mfma_f32_16x16x32_bf16 v[20:23], v[152:155], v[202:205], v[20:23]
	v_mfma_f32_16x16x32_bf16 v[20:23], v[156:159], v[206:209], v[20:23]
	v_mfma_f32_16x16x32_bf16 v[4:7], v[152:155], v[216:219], v[4:7]
	v_mfma_f32_16x16x32_bf16 v[4:7], v[156:159], v[220:223], v[4:7]
	v_mfma_f32_16x16x32_bf16 v[64:67], v[164:167], v[180:183], v[64:67]
	v_mfma_f32_16x16x32_bf16 v[64:67], v[168:171], v[190:193], v[64:67]
	v_mfma_f32_16x16x32_bf16 v[48:51], v[164:167], v[194:197], v[48:51]
	v_mfma_f32_16x16x32_bf16 v[48:51], v[168:171], v[198:201], v[48:51]
	v_mfma_f32_16x16x32_bf16 v[32:35], v[164:167], v[202:205], v[32:35]
	v_mfma_f32_16x16x32_bf16 v[32:35], v[168:171], v[206:209], v[32:35]
	v_mfma_f32_16x16x32_bf16 v[16:19], v[164:167], v[216:219], v[16:19]
	v_mfma_f32_16x16x32_bf16 v[16:19], v[168:171], v[220:223], v[16:19]
	v_mfma_f32_16x16x32_bf16 v[60:63], v[172:175], v[180:183], v[60:63]
	v_mfma_f32_16x16x32_bf16 v[60:63], v[176:179], v[190:193], v[60:63]
	v_mfma_f32_16x16x32_bf16 v[44:47], v[172:175], v[194:197], v[44:47]
	v_mfma_f32_16x16x32_bf16 v[44:47], v[176:179], v[198:201], v[44:47]
	v_mfma_f32_16x16x32_bf16 v[28:31], v[172:175], v[202:205], v[28:31]
	v_mfma_f32_16x16x32_bf16 v[28:31], v[176:179], v[206:209], v[28:31]
	v_mfma_f32_16x16x32_bf16 v[12:15], v[172:175], v[216:219], v[12:15]
	v_mfma_f32_16x16x32_bf16 v[12:15], v[176:179], v[220:223], v[12:15]
	s_barrier
	s_add_i32 s30, s30, 2
	s_add_u32 s10, s10, 0x100
	s_addc_u32 s11, s11, 0
	s_add_u32 s28, s28, 0x100
	s_addc_u32 s29, s29, 0
	s_cmp_gt_u32 s30, 29
	s_cbranch_scc0 .LBB0_130
	s_and_b64 vcc, exec, s[20:21]
	s_cbranch_vccz .LBB0_133
	s_barrier

.LBB0_233:
	ds_read_b128 v[120:123], v116
	ds_read_b128 v[132:135], v116 offset:1024
	ds_read_b128 v[144:147], v116 offset:2048
	ds_read_b128 v[148:151], v116 offset:3072
	ds_read_b128 v[152:155], v117
	ds_read_b128 v[156:159], v117 offset:1024
	ds_read_b128 v[166:169], v117 offset:2048
	ds_read_b128 v[170:173], v117 offset:3072
	s_add_u32 s49, s26, 0xffea0080
	s_addc_u32 s50, s27, -1
	s_cmpk_eq_i32 s48, 0x54
	s_cselect_b32 s51, s21, s50
	s_cselect_b32 s50, s20, s49
	s_cselect_b32 s53, s23, s25
	s_cselect_b32 s52, s22, s24
	s_mov_b32 m0, s0
	v_lshl_add_u64 v[188:189], s[26:27], 0, v[164:165]
	ds_read_b128 v[180:183], v178
	ds_read_b128 v[184:187], v178 offset:1024
	ds_read_b128 v[190:193], v178 offset:2048
	ds_read_b128 v[194:197], v178 offset:3072
	ds_read_b128 v[198:201], v178 offset:4096
	ds_read_b128 v[202:205], v178 offset:5120
	ds_read_b128 v[206:209], v178 offset:6144
	ds_read_b128 v[216:219], v178 offset:7168
	global_load_lds_dwordx4 v[188:189], off
	v_lshl_add_u64 v[188:189], v[188:189], 0, s[86:87]
	s_mov_b32 m0, s4
	s_nop 0
	global_load_lds_dwordx4 v[188:189], off
	s_waitcnt vmcnt(8)
	s_waitcnt lgkmcnt(0)
	s_barrier
	v_mfma_f32_16x16x32_bf16 v[140:143], v[120:123], v[180:183], v[140:143]
	v_mfma_f32_16x16x32_bf16 v[140:143], v[132:135], v[184:187], v[140:143]
	v_mfma_f32_16x16x32_bf16 v[112:115], v[120:123], v[190:193], v[112:115]
	v_mfma_f32_16x16x32_bf16 v[112:115], v[132:135], v[194:197], v[112:115]
	v_mfma_f32_16x16x32_bf16 v[96:99], v[120:123], v[198:201], v[96:99]
	v_mfma_f32_16x16x32_bf16 v[96:99], v[132:135], v[202:205], v[96:99]
	v_mfma_f32_16x16x32_bf16 v[80:83], v[120:123], v[206:209], v[80:83]
	v_mfma_f32_16x16x32_bf16 v[80:83], v[132:135], v[216:219], v[80:83]
	v_mfma_f32_16x16x32_bf16 v[136:139], v[144:147], v[180:183], v[136:139]
	v_mfma_f32_16x16x32_bf16 v[136:139], v[148:151], v[184:187], v[136:139]
	v_mfma_f32_16x16x32_bf16 v[108:111], v[144:147], v[190:193], v[108:111]
	v_mfma_f32_16x16x32_bf16 v[108:111], v[148:151], v[194:197], v[108:111]
	v_mfma_f32_16x16x32_bf16 v[92:95], v[144:147], v[198:201], v[92:95]
	v_mfma_f32_16x16x32_bf16 v[92:95], v[148:151], v[202:205], v[92:95]
	v_mfma_f32_16x16x32_bf16 v[76:79], v[144:147], v[206:209], v[76:79]
	v_mfma_f32_16x16x32_bf16 v[76:79], v[148:151], v[216:219], v[76:79]
	v_mfma_f32_16x16x32_bf16 v[128:131], v[152:155], v[180:183], v[128:131]
	v_mfma_f32_16x16x32_bf16 v[128:131], v[156:159], v[184:187], v[128:131]
	v_mfma_f32_16x16x32_bf16 v[104:107], v[152:155], v[190:193], v[104:107]
	v_mfma_f32_16x16x32_bf16 v[104:107], v[156:159], v[194:197], v[104:107]
	v_mfma_f32_16x16x32_bf16 v[88:91], v[152:155], v[198:201], v[88:91]
	v_mfma_f32_16x16x32_bf16 v[88:91], v[156:159], v[202:205], v[88:91]
	v_mfma_f32_16x16x32_bf16 v[72:75], v[152:155], v[206:209], v[72:75]
	v_mfma_f32_16x16x32_bf16 v[72:75], v[156:159], v[216:219], v[72:75]
	v_mfma_f32_16x16x32_bf16 v[124:127], v[166:169], v[180:183], v[124:127]
	v_mfma_f32_16x16x32_bf16 v[124:127], v[170:173], v[184:187], v[124:127]
	v_mfma_f32_16x16x32_bf16 v[100:103], v[166:169], v[190:193], v[100:103]
	v_mfma_f32_16x16x32_bf16 v[100:103], v[170:173], v[194:197], v[100:103]
	v_mfma_f32_16x16x32_bf16 v[84:87], v[166:169], v[198:201], v[84:87]
	v_mfma_f32_16x16x32_bf16 v[84:87], v[170:173], v[202:205], v[84:87]
	v_mfma_f32_16x16x32_bf16 v[68:71], v[166:169], v[206:209], v[68:71]
	v_mfma_f32_16x16x32_bf16 v[68:71], v[170:173], v[216:219], v[68:71]
	s_barrier
	s_mov_b32 m0, s5
	v_lshl_add_u64 v[188:189], s[52:53], 0, v[162:163]
	ds_read_b128 v[180:183], v178 offset:16384
	ds_read_b128 v[184:187], v178 offset:17408
	ds_read_b128 v[190:193], v178 offset:18432
	ds_read_b128 v[194:197], v178 offset:19456
	ds_read_b128 v[198:201], v178 offset:20480
	ds_read_b128 v[202:205], v178 offset:21504
	ds_read_b128 v[206:209], v178 offset:22528
	ds_read_b128 v[216:219], v178 offset:23552
	global_load_lds_dwordx4 v[188:189], off
	v_lshl_add_u64 v[214:215], v[188:189], 0, s[86:87]
	s_mov_b32 m0, s33
	s_nop 0
	global_load_lds_dwordx4 v[214:215], off
	v_lshl_add_u64 v[214:215], v[188:189], 0, s[54:55]
	s_mov_b32 m0, s42
	s_nop 0
	global_load_lds_dwordx4 v[214:215], off
	v_lshl_add_u64 v[214:215], v[188:189], 0, s[56:57]
	s_mov_b32 m0, s43
	s_nop 0
	global_load_lds_dwordx4 v[214:215], off
	v_lshl_add_u64 v[214:215], s[50:51], 0, v[160:161]
	s_mov_b32 m0, s31
	v_lshl_add_u64 v[220:221], v[214:215], 0, s[86:87]
	global_load_lds_dwordx4 v[214:215], off
	s_mov_b32 m0, s34
	s_nop 0
	global_load_lds_dwordx4 v[220:221], off
	s_waitcnt vmcnt(8)
	s_waitcnt lgkmcnt(0)
	s_barrier
	v_mfma_f32_16x16x32_bf16 v[56:59], v[120:123], v[180:183], v[56:59]
	v_mfma_f32_16x16x32_bf16 v[56:59], v[132:135], v[184:187], v[56:59]
	v_mfma_f32_16x16x32_bf16 v[48:51], v[120:123], v[190:193], v[48:51]
	v_mfma_f32_16x16x32_bf16 v[48:51], v[132:135], v[194:197], v[48:51]
	v_mfma_f32_16x16x32_bf16 v[32:35], v[120:123], v[198:201], v[32:35]
	v_mfma_f32_16x16x32_bf16 v[32:35], v[132:135], v[202:205], v[32:35]
	v_mfma_f32_16x16x32_bf16 v[16:19], v[120:123], v[206:209], v[16:19]
	v_mfma_f32_16x16x32_bf16 v[16:19], v[132:135], v[216:219], v[16:19]
	v_mfma_f32_16x16x32_bf16 v[52:55], v[144:147], v[180:183], v[52:55]
	v_mfma_f32_16x16x32_bf16 v[52:55], v[148:151], v[184:187], v[52:55]
	v_mfma_f32_16x16x32_bf16 v[44:47], v[144:147], v[190:193], v[44:47]
	v_mfma_f32_16x16x32_bf16 v[44:47], v[148:151], v[194:197], v[44:47]
	v_mfma_f32_16x16x32_bf16 v[28:31], v[144:147], v[198:201], v[28:31]
	v_mfma_f32_16x16x32_bf16 v[28:31], v[148:151], v[202:205], v[28:31]
	v_mfma_f32_16x16x32_bf16 v[12:15], v[144:147], v[206:209], v[12:15]
	v_mfma_f32_16x16x32_bf16 v[12:15], v[148:151], v[216:219], v[12:15]
	v_mfma_f32_16x16x32_bf16 v[64:67], v[152:155], v[180:183], v[64:67]
	v_mfma_f32_16x16x32_bf16 v[64:67], v[156:159], v[184:187], v[64:67]
	v_mfma_f32_16x16x32_bf16 v[40:43], v[152:155], v[190:193], v[40:43]
	v_mfma_f32_16x16x32_bf16 v[40:43], v[156:159], v[194:197], v[40:43]
	v_mfma_f32_16x16x32_bf16 v[24:27], v[152:155], v[198:201], v[24:27]
	v_mfma_f32_16x16x32_bf16 v[24:27], v[156:159], v[202:205], v[24:27]
	v_mfma_f32_16x16x32_bf16 v[8:11], v[152:155], v[206:209], v[8:11]
	v_mfma_f32_16x16x32_bf16 v[8:11], v[156:159], v[216:219], v[8:11]
	v_mfma_f32_16x16x32_bf16 v[60:63], v[166:169], v[180:183], v[60:63]
	v_mfma_f32_16x16x32_bf16 v[60:63], v[170:173], v[184:187], v[60:63]
	v_mfma_f32_16x16x32_bf16 v[36:39], v[166:169], v[190:193], v[36:39]
	v_mfma_f32_16x16x32_bf16 v[36:39], v[170:173], v[194:197], v[36:39]
	v_mfma_f32_16x16x32_bf16 v[20:23], v[166:169], v[198:201], v[20:23]
	v_mfma_f32_16x16x32_bf16 v[20:23], v[170:173], v[202:205], v[20:23]
	v_mfma_f32_16x16x32_bf16 v[4:7], v[166:169], v[206:209], v[4:7]
	v_mfma_f32_16x16x32_bf16 v[4:7], v[170:173], v[216:219], v[4:7]
	s_barrier
	ds_read_b128 v[120:123], v118
	ds_read_b128 v[132:135], v118 offset:1024
	ds_read_b128 v[144:147], v118 offset:2048
	ds_read_b128 v[148:151], v118 offset:3072
	ds_read_b128 v[152:155], v119
	ds_read_b128 v[156:159], v119 offset:1024
	ds_read_b128 v[166:169], v119 offset:2048
	ds_read_b128 v[170:173], v119 offset:3072
	s_mov_b32 m0, s35
	v_lshl_add_u64 v[220:221], v[214:215], 0, s[54:55]
	ds_read_b128 v[180:183], v178 offset:32768
	ds_read_b128 v[184:187], v178 offset:33792
	ds_read_b128 v[190:193], v178 offset:34816
	ds_read_b128 v[194:197], v178 offset:35840
	ds_read_b128 v[198:201], v178 offset:36864
	ds_read_b128 v[202:205], v178 offset:37888
	ds_read_b128 v[206:209], v178 offset:38912
	ds_read_b128 v[216:219], v178 offset:39936
	global_load_lds_dwordx4 v[220:221], off
	v_lshl_add_u64 v[220:221], v[214:215], 0, s[56:57]
	s_mov_b32 m0, s36
	s_nop 0
	global_load_lds_dwordx4 v[220:221], off
	s_waitcnt vmcnt(8)
	s_waitcnt lgkmcnt(0)
	s_barrier
	v_mfma_f32_16x16x32_bf16 v[140:143], v[120:123], v[180:183], v[140:143]
	v_mfma_f32_16x16x32_bf16 v[140:143], v[132:135], v[184:187], v[140:143]
	v_mfma_f32_16x16x32_bf16 v[112:115], v[120:123], v[190:193], v[112:115]
	v_mfma_f32_16x16x32_bf16 v[112:115], v[132:135], v[194:197], v[112:115]
	v_mfma_f32_16x16x32_bf16 v[96:99], v[120:123], v[198:201], v[96:99]
	v_mfma_f32_16x16x32_bf16 v[96:99], v[132:135], v[202:205], v[96:99]
	v_mfma_f32_16x16x32_bf16 v[80:83], v[120:123], v[206:209], v[80:83]
	v_mfma_f32_16x16x32_bf16 v[80:83], v[132:135], v[216:219], v[80:83]
	v_mfma_f32_16x16x32_bf16 v[136:139], v[144:147], v[180:183], v[136:139]
	v_mfma_f32_16x16x32_bf16 v[136:139], v[148:151], v[184:187], v[136:139]
	v_mfma_f32_16x16x32_bf16 v[108:111], v[144:147], v[190:193], v[108:111]
	v_mfma_f32_16x16x32_bf16 v[108:111], v[148:151], v[194:197], v[108:111]
	v_mfma_f32_16x16x32_bf16 v[92:95], v[144:147], v[198:201], v[92:95]
	v_mfma_f32_16x16x32_bf16 v[92:95], v[148:151], v[202:205], v[92:95]
	v_mfma_f32_16x16x32_bf16 v[76:79], v[144:147], v[206:209], v[76:79]
	v_mfma_f32_16x16x32_bf16 v[76:79], v[148:151], v[216:219], v[76:79]
	v_mfma_f32_16x16x32_bf16 v[128:131], v[152:155], v[180:183], v[128:131]
	v_mfma_f32_16x16x32_bf16 v[128:131], v[156:159], v[184:187], v[128:131]
	v_mfma_f32_16x16x32_bf16 v[104:107], v[152:155], v[190:193], v[104:107]
	v_mfma_f32_16x16x32_bf16 v[104:107], v[156:159], v[194:197], v[104:107]
	v_mfma_f32_16x16x32_bf16 v[88:91], v[152:155], v[198:201], v[88:91]
	v_mfma_f32_16x16x32_bf16 v[88:91], v[156:159], v[202:205], v[88:91]
	v_mfma_f32_16x16x32_bf16 v[72:75], v[152:155], v[206:209], v[72:75]
	v_mfma_f32_16x16x32_bf16 v[72:75], v[156:159], v[216:219], v[72:75]
	v_mfma_f32_16x16x32_bf16 v[124:127], v[166:169], v[180:183], v[124:127]
	v_mfma_f32_16x16x32_bf16 v[124:127], v[170:173], v[184:187], v[124:127]
	v_mfma_f32_16x16x32_bf16 v[100:103], v[166:169], v[190:193], v[100:103]
	v_mfma_f32_16x16x32_bf16 v[100:103], v[170:173], v[194:197], v[100:103]
	v_mfma_f32_16x16x32_bf16 v[84:87], v[166:169], v[198:201], v[84:87]
	v_mfma_f32_16x16x32_bf16 v[84:87], v[170:173], v[202:205], v[84:87]
	v_mfma_f32_16x16x32_bf16 v[68:71], v[166:169], v[206:209], v[68:71]
	v_mfma_f32_16x16x32_bf16 v[68:71], v[170:173], v[216:219], v[68:71]
	s_barrier
; #define PG8_MMA(ai, bj, At, Bt) do { __builtin_amdgcn_s_setprio(1); _Pragma("unroll") for (int m = 0; m < 4; ++m) _Pragma("unroll") for (int n = 0; n < 2; ++n) _Pragma("unroll") for (int k = 0; k < 2; ++k) \
;         acc[ai][bj][m][n] = __builtin_amdgcn_mfma_f32_16x16x32_bf16(Bt[n][k], At[m][k], acc[ai][bj][m][n], 0, 0, 0); __builtin_amdgcn_s_setprio(0); } while (0)
; #define PG8_WAIT_V(n) asm volatile("s_waitcnt vmcnt(" #n ")" ::: "memory")
; #define PG8_TRIP_HEAD(T) const int t = (T); const bool last = (t == nt - 2); \
;             const char* a1 = cA + (size_t)(t + 1) * kstep; \
;             const char* a2 = last ? nA : cA + (size_t)(t + 2) * kstep; const char* b2 = last ? nB : cB + (size_t)(t + 2) * kstep; \
;             const char* a3 = a2 + kstep; const char* b3 = b2 + kstep; \
;             if (last && has_next) S.a_ready(nxt);
; template <class Epi, class Sched, bool ALIGN_EPI = false, bool SP2 = false>
; __device__ __forceinline__ void gemm_phase(PG8_LAS unsigned char* lds, const Gemm g, const Sched& S, const Epi& E) {
;     ...
;         if constexpr (SP2) {
;             { PG8_TRIP_HEAD(0) PG8_TRIP_SP2(asm volatile("s_waitcnt vmcnt(%0)" :: "n"(8 + Epi::NST) : "memory"), PG8_MMAZ) }
;             for (int tt = 2; tt < nt; tt += 2) { PG8_TRIP_HEAD(tt) PG8_TRIP_SP2(PG8_WAIT_V(8), PG8_MMA) }
	s_mov_b32 m0, s44
	v_lshl_add_u64 v[220:221], v[188:189], 0, s[78:79]
	ds_read_b128 v[180:183], v178 offset:49152
	ds_read_b128 v[184:187], v178 offset:50176
	ds_read_b128 v[190:193], v178 offset:51200
	ds_read_b128 v[194:197], v178 offset:52224
	ds_read_b128 v[198:201], v178 offset:53248
	ds_read_b128 v[202:205], v178 offset:54272
	ds_read_b128 v[206:209], v178 offset:55296
	ds_read_b128 v[216:219], v178 offset:56320
	global_load_lds_dwordx4 v[220:221], off
	v_lshl_add_u64 v[220:221], v[188:189], 0, s[60:61]
	s_mov_b32 m0, s45
	s_nop 0
	global_load_lds_dwordx4 v[220:221], off
	v_lshl_add_u64 v[220:221], v[188:189], 0, s[62:63]
	s_mov_b32 m0, s46
	v_lshl_add_u64 v[188:189], v[188:189], 0, s[64:65]
	global_load_lds_dwordx4 v[220:221], off
	s_mov_b32 m0, s47
	s_nop 0
	global_load_lds_dwordx4 v[188:189], off
	v_lshl_add_u64 v[188:189], v[214:215], 0, s[78:79]
	s_mov_b32 m0, s37
	s_nop 0
	global_load_lds_dwordx4 v[188:189], off
	v_lshl_add_u64 v[188:189], v[214:215], 0, s[60:61]
	s_mov_b32 m0, s38
	s_nop 0
	global_load_lds_dwordx4 v[188:189], off
	s_waitcnt vmcnt(8)
	s_waitcnt lgkmcnt(0)
	s_barrier
	v_mfma_f32_16x16x32_bf16 v[56:59], v[120:123], v[180:183], v[56:59]
	v_mfma_f32_16x16x32_bf16 v[56:59], v[132:135], v[184:187], v[56:59]
	v_mfma_f32_16x16x32_bf16 v[48:51], v[120:123], v[190:193], v[48:51]
	v_mfma_f32_16x16x32_bf16 v[48:51], v[132:135], v[194:197], v[48:51]
	v_mfma_f32_16x16x32_bf16 v[32:35], v[120:123], v[198:201], v[32:35]
	v_mfma_f32_16x16x32_bf16 v[32:35], v[132:135], v[202:205], v[32:35]
	v_mfma_f32_16x16x32_bf16 v[16:19], v[120:123], v[206:209], v[16:19]
	v_mfma_f32_16x16x32_bf16 v[16:19], v[132:135], v[216:219], v[16:19]
	v_mfma_f32_16x16x32_bf16 v[52:55], v[144:147], v[180:183], v[52:55]
	v_mfma_f32_16x16x32_bf16 v[52:55], v[148:151], v[184:187], v[52:55]
	v_mfma_f32_16x16x32_bf16 v[44:47], v[144:147], v[190:193], v[44:47]
	v_mfma_f32_16x16x32_bf16 v[44:47], v[148:151], v[194:197], v[44:47]
	v_mfma_f32_16x16x32_bf16 v[28:31], v[144:147], v[198:201], v[28:31]
	v_mfma_f32_16x16x32_bf16 v[28:31], v[148:151], v[202:205], v[28:31]
	v_mfma_f32_16x16x32_bf16 v[12:15], v[144:147], v[206:209], v[12:15]
	v_mfma_f32_16x16x32_bf16 v[12:15], v[148:151], v[216:219], v[12:15]
	v_mfma_f32_16x16x32_bf16 v[64:67], v[152:155], v[180:183], v[64:67]
	v_mfma_f32_16x16x32_bf16 v[64:67], v[156:159], v[184:187], v[64:67]
	v_mfma_f32_16x16x32_bf16 v[40:43], v[152:155], v[190:193], v[40:43]
	v_mfma_f32_16x16x32_bf16 v[40:43], v[156:159], v[194:197], v[40:43]
	v_mfma_f32_16x16x32_bf16 v[24:27], v[152:155], v[198:201], v[24:27]
	v_mfma_f32_16x16x32_bf16 v[24:27], v[156:159], v[202:205], v[24:27]
	v_mfma_f32_16x16x32_bf16 v[8:11], v[152:155], v[206:209], v[8:11]
	v_mfma_f32_16x16x32_bf16 v[8:11], v[156:159], v[216:219], v[8:11]
	v_mfma_f32_16x16x32_bf16 v[60:63], v[166:169], v[180:183], v[60:63]
	v_mfma_f32_16x16x32_bf16 v[60:63], v[170:173], v[184:187], v[60:63]
	v_mfma_f32_16x16x32_bf16 v[36:39], v[166:169], v[190:193], v[36:39]
	v_mfma_f32_16x16x32_bf16 v[36:39], v[170:173], v[194:197], v[36:39]
	v_mfma_f32_16x16x32_bf16 v[20:23], v[166:169], v[198:201], v[20:23]
	v_mfma_f32_16x16x32_bf16 v[20:23], v[170:173], v[202:205], v[20:23]
	v_mfma_f32_16x16x32_bf16 v[4:7], v[166:169], v[206:209], v[4:7]
	v_mfma_f32_16x16x32_bf16 v[4:7], v[170:173], v[216:219], v[4:7]
	s_barrier
	s_add_i32 s48, s48, 2
	s_add_u32 s26, s26, 0x100
	s_addc_u32 s27, s27, 0
	s_add_u32 s24, s24, 0x100
	s_addc_u32 s25, s25, 0
	s_cmpk_gt_u32 s48, 0x55
	s_cbranch_scc0 .LBB0_233
	s_and_b64 vcc, exec, s[18:19]
	s_cbranch_vccz .LBB0_236
	s_barrier

.LBB0_324:
	ds_read_b128 v[136:139], v132
	ds_read_b128 v[140:143], v132 offset:1024
	ds_read_b128 v[144:147], v132 offset:2048
	ds_read_b128 v[148:151], v132 offset:3072
	ds_read_b128 v[152:155], v133
	ds_read_b128 v[156:159], v133 offset:1024
	ds_read_b128 v[160:163], v133 offset:2048
	ds_read_b128 v[174:177], v133 offset:3072
	s_add_u32 s15, s10, 0xfff7c080
	s_addc_u32 s50, s11, -1
	s_cmp_eq_u32 s14, 28
	s_cselect_b32 s51, s25, s50
	s_cselect_b32 s50, s24, s15
	s_cselect_b32 s53, s3, s13
	s_cselect_b32 s52, s4, s12
	s_mov_b32 m0, s5
	v_lshl_add_u64 v[194:195], s[10:11], 0, v[172:173]
	ds_read_b128 v[178:181], v200
	ds_read_b128 v[182:185], v200 offset:1024
	ds_read_b128 v[186:189], v200 offset:2048
	ds_read_b128 v[190:193], v200 offset:3072
	ds_read_b128 v[202:205], v200 offset:4096
	ds_read_b128 v[206:209], v200 offset:5120
	ds_read_b128 v[216:219], v200 offset:6144
	ds_read_b128 v[220:223], v200 offset:7168
	global_load_lds_dwordx4 v[194:195], off
	v_lshl_add_u64 v[194:195], v[194:195], 0, s[96:97]
	s_mov_b32 m0, s23
	s_nop 0
	global_load_lds_dwordx4 v[194:195], off
	s_waitcnt vmcnt(8)
	s_waitcnt lgkmcnt(0)
	s_barrier
	v_mfma_f32_16x16x32_bf16 v[120:123], v[136:139], v[178:181], v[120:123]
	v_mfma_f32_16x16x32_bf16 v[120:123], v[140:143], v[182:185], v[120:123]
	v_mfma_f32_16x16x32_bf16 v[104:107], v[136:139], v[186:189], v[104:107]
	v_mfma_f32_16x16x32_bf16 v[104:107], v[140:143], v[190:193], v[104:107]
	v_mfma_f32_16x16x32_bf16 v[88:91], v[136:139], v[202:205], v[88:91]
	v_mfma_f32_16x16x32_bf16 v[88:91], v[140:143], v[206:209], v[88:91]
	v_mfma_f32_16x16x32_bf16 v[72:75], v[136:139], v[216:219], v[72:75]
	v_mfma_f32_16x16x32_bf16 v[72:75], v[140:143], v[220:223], v[72:75]
	v_mfma_f32_16x16x32_bf16 v[116:119], v[144:147], v[178:181], v[116:119]
	v_mfma_f32_16x16x32_bf16 v[116:119], v[148:151], v[182:185], v[116:119]
	v_mfma_f32_16x16x32_bf16 v[100:103], v[144:147], v[186:189], v[100:103]
	v_mfma_f32_16x16x32_bf16 v[100:103], v[148:151], v[190:193], v[100:103]
	v_mfma_f32_16x16x32_bf16 v[84:87], v[144:147], v[202:205], v[84:87]
	v_mfma_f32_16x16x32_bf16 v[84:87], v[148:151], v[206:209], v[84:87]
	v_mfma_f32_16x16x32_bf16 v[68:71], v[144:147], v[216:219], v[68:71]
	v_mfma_f32_16x16x32_bf16 v[68:71], v[148:151], v[220:223], v[68:71]
	v_mfma_f32_16x16x32_bf16 v[128:131], v[152:155], v[178:181], v[128:131]
	v_mfma_f32_16x16x32_bf16 v[128:131], v[156:159], v[182:185], v[128:131]
	v_mfma_f32_16x16x32_bf16 v[112:115], v[152:155], v[186:189], v[112:115]
	v_mfma_f32_16x16x32_bf16 v[112:115], v[156:159], v[190:193], v[112:115]
	v_mfma_f32_16x16x32_bf16 v[96:99], v[152:155], v[202:205], v[96:99]
	v_mfma_f32_16x16x32_bf16 v[96:99], v[156:159], v[206:209], v[96:99]
	v_mfma_f32_16x16x32_bf16 v[80:83], v[152:155], v[216:219], v[80:83]
	v_mfma_f32_16x16x32_bf16 v[80:83], v[156:159], v[220:223], v[80:83]
	v_mfma_f32_16x16x32_bf16 v[124:127], v[160:163], v[178:181], v[124:127]
	v_mfma_f32_16x16x32_bf16 v[124:127], v[174:177], v[182:185], v[124:127]
	v_mfma_f32_16x16x32_bf16 v[108:111], v[160:163], v[186:189], v[108:111]
	v_mfma_f32_16x16x32_bf16 v[108:111], v[174:177], v[190:193], v[108:111]
	v_mfma_f32_16x16x32_bf16 v[92:95], v[160:163], v[202:205], v[92:95]
	v_mfma_f32_16x16x32_bf16 v[92:95], v[174:177], v[206:209], v[92:95]
	v_mfma_f32_16x16x32_bf16 v[76:79], v[160:163], v[216:219], v[76:79]
	v_mfma_f32_16x16x32_bf16 v[76:79], v[174:177], v[220:223], v[76:79]
	s_barrier
	s_mov_b32 m0, s28
	v_lshl_add_u64 v[194:195], s[52:53], 0, v[164:165]
	ds_read_b128 v[178:181], v200 offset:16384
	ds_read_b128 v[182:185], v200 offset:17408
	ds_read_b128 v[186:189], v200 offset:18432
	ds_read_b128 v[190:193], v200 offset:19456
	ds_read_b128 v[202:205], v200 offset:20480
	ds_read_b128 v[206:209], v200 offset:21504
	ds_read_b128 v[216:219], v200 offset:22528
	ds_read_b128 v[220:223], v200 offset:23552
	global_load_lds_dwordx4 v[194:195], off
	v_lshl_add_u64 v[214:215], v[194:195], 0, s[90:91]
	s_mov_b32 m0, s29
	s_nop 0
	global_load_lds_dwordx4 v[214:215], off
	v_lshl_add_u64 v[214:215], v[194:195], 0, s[54:55]
	s_mov_b32 m0, s33
	s_nop 0
	global_load_lds_dwordx4 v[214:215], off
	v_lshl_add_u64 v[214:215], v[194:195], 0, s[60:61]
	s_mov_b32 m0, s45
	s_nop 0
	global_load_lds_dwordx4 v[214:215], off
	v_lshl_add_u64 v[214:215], s[50:51], 0, v[166:167]
	s_mov_b32 m0, s30
	v_lshl_add_u64 v[224:225], v[214:215], 0, s[96:97]
	global_load_lds_dwordx4 v[214:215], off
	s_mov_b32 m0, s31
	s_nop 0
	global_load_lds_dwordx4 v[224:225], off
	s_waitcnt vmcnt(8)
	s_waitcnt lgkmcnt(0)
	s_barrier
	v_mfma_f32_16x16x32_bf16 v[56:59], v[136:139], v[178:181], v[56:59]
	v_mfma_f32_16x16x32_bf16 v[56:59], v[140:143], v[182:185], v[56:59]
	v_mfma_f32_16x16x32_bf16 v[40:43], v[136:139], v[186:189], v[40:43]
	v_mfma_f32_16x16x32_bf16 v[40:43], v[140:143], v[190:193], v[40:43]
	v_mfma_f32_16x16x32_bf16 v[24:27], v[136:139], v[202:205], v[24:27]
	v_mfma_f32_16x16x32_bf16 v[24:27], v[140:143], v[206:209], v[24:27]
	v_mfma_f32_16x16x32_bf16 v[8:11], v[136:139], v[216:219], v[8:11]
	v_mfma_f32_16x16x32_bf16 v[8:11], v[140:143], v[220:223], v[8:11]
	v_mfma_f32_16x16x32_bf16 v[52:55], v[144:147], v[178:181], v[52:55]
	v_mfma_f32_16x16x32_bf16 v[52:55], v[148:151], v[182:185], v[52:55]
	v_mfma_f32_16x16x32_bf16 v[36:39], v[144:147], v[186:189], v[36:39]
	v_mfma_f32_16x16x32_bf16 v[36:39], v[148:151], v[190:193], v[36:39]
	v_mfma_f32_16x16x32_bf16 v[20:23], v[144:147], v[202:205], v[20:23]
	v_mfma_f32_16x16x32_bf16 v[20:23], v[148:151], v[206:209], v[20:23]
	v_mfma_f32_16x16x32_bf16 v[4:7], v[144:147], v[216:219], v[4:7]
	v_mfma_f32_16x16x32_bf16 v[4:7], v[148:151], v[220:223], v[4:7]
	v_mfma_f32_16x16x32_bf16 v[64:67], v[152:155], v[178:181], v[64:67]
	v_mfma_f32_16x16x32_bf16 v[64:67], v[156:159], v[182:185], v[64:67]
	v_mfma_f32_16x16x32_bf16 v[48:51], v[152:155], v[186:189], v[48:51]
	v_mfma_f32_16x16x32_bf16 v[48:51], v[156:159], v[190:193], v[48:51]
	v_mfma_f32_16x16x32_bf16 v[32:35], v[152:155], v[202:205], v[32:35]
	v_mfma_f32_16x16x32_bf16 v[32:35], v[156:159], v[206:209], v[32:35]
	v_mfma_f32_16x16x32_bf16 v[16:19], v[152:155], v[216:219], v[16:19]
	v_mfma_f32_16x16x32_bf16 v[16:19], v[156:159], v[220:223], v[16:19]
	v_mfma_f32_16x16x32_bf16 v[60:63], v[160:163], v[178:181], v[60:63]
	v_mfma_f32_16x16x32_bf16 v[60:63], v[174:177], v[182:185], v[60:63]
	v_mfma_f32_16x16x32_bf16 v[44:47], v[160:163], v[186:189], v[44:47]
	v_mfma_f32_16x16x32_bf16 v[44:47], v[174:177], v[190:193], v[44:47]
	v_mfma_f32_16x16x32_bf16 v[28:31], v[160:163], v[202:205], v[28:31]
	v_mfma_f32_16x16x32_bf16 v[28:31], v[174:177], v[206:209], v[28:31]
	v_mfma_f32_16x16x32_bf16 v[12:15], v[160:163], v[216:219], v[12:15]
	v_mfma_f32_16x16x32_bf16 v[12:15], v[174:177], v[220:223], v[12:15]
	s_barrier
	ds_read_b128 v[136:139], v134
	ds_read_b128 v[140:143], v134 offset:1024
	ds_read_b128 v[144:147], v134 offset:2048
	ds_read_b128 v[148:151], v134 offset:3072
	ds_read_b128 v[152:155], v135
	ds_read_b128 v[156:159], v135 offset:1024
	ds_read_b128 v[160:163], v135 offset:2048
	ds_read_b128 v[174:177], v135 offset:3072
	s_mov_b32 m0, s34
	v_lshl_add_u64 v[224:225], v[214:215], 0, s[82:83]
	ds_read_b128 v[178:181], v200 offset:32768
	ds_read_b128 v[182:185], v200 offset:33792
	ds_read_b128 v[186:189], v200 offset:34816
	ds_read_b128 v[190:193], v200 offset:35840
	ds_read_b128 v[202:205], v200 offset:36864
	ds_read_b128 v[206:209], v200 offset:37888
	ds_read_b128 v[216:219], v200 offset:38912
	ds_read_b128 v[220:223], v200 offset:39936
	global_load_lds_dwordx4 v[224:225], off
	v_lshl_add_u64 v[224:225], v[214:215], 0, s[64:65]
	s_mov_b32 m0, s35
	s_nop 0
	global_load_lds_dwordx4 v[224:225], off
	s_waitcnt vmcnt(8)
	s_waitcnt lgkmcnt(0)
	s_barrier
	v_mfma_f32_16x16x32_bf16 v[120:123], v[136:139], v[178:181], v[120:123]
	v_mfma_f32_16x16x32_bf16 v[120:123], v[140:143], v[182:185], v[120:123]
	v_mfma_f32_16x16x32_bf16 v[104:107], v[136:139], v[186:189], v[104:107]
	v_mfma_f32_16x16x32_bf16 v[104:107], v[140:143], v[190:193], v[104:107]
	v_mfma_f32_16x16x32_bf16 v[88:91], v[136:139], v[202:205], v[88:91]
	v_mfma_f32_16x16x32_bf16 v[88:91], v[140:143], v[206:209], v[88:91]
	v_mfma_f32_16x16x32_bf16 v[72:75], v[136:139], v[216:219], v[72:75]
	v_mfma_f32_16x16x32_bf16 v[72:75], v[140:143], v[220:223], v[72:75]
	v_mfma_f32_16x16x32_bf16 v[116:119], v[144:147], v[178:181], v[116:119]
	v_mfma_f32_16x16x32_bf16 v[116:119], v[148:151], v[182:185], v[116:119]
	v_mfma_f32_16x16x32_bf16 v[100:103], v[144:147], v[186:189], v[100:103]
	v_mfma_f32_16x16x32_bf16 v[100:103], v[148:151], v[190:193], v[100:103]
	v_mfma_f32_16x16x32_bf16 v[84:87], v[144:147], v[202:205], v[84:87]
	v_mfma_f32_16x16x32_bf16 v[84:87], v[148:151], v[206:209], v[84:87]
	v_mfma_f32_16x16x32_bf16 v[68:71], v[144:147], v[216:219], v[68:71]
	v_mfma_f32_16x16x32_bf16 v[68:71], v[148:151], v[220:223], v[68:71]
	v_mfma_f32_16x16x32_bf16 v[128:131], v[152:155], v[178:181], v[128:131]
	v_mfma_f32_16x16x32_bf16 v[128:131], v[156:159], v[182:185], v[128:131]
	v_mfma_f32_16x16x32_bf16 v[112:115], v[152:155], v[186:189], v[112:115]
	v_mfma_f32_16x16x32_bf16 v[112:115], v[156:159], v[190:193], v[112:115]
	v_mfma_f32_16x16x32_bf16 v[96:99], v[152:155], v[202:205], v[96:99]
	v_mfma_f32_16x16x32_bf16 v[96:99], v[156:159], v[206:209], v[96:99]
	v_mfma_f32_16x16x32_bf16 v[80:83], v[152:155], v[216:219], v[80:83]
	v_mfma_f32_16x16x32_bf16 v[80:83], v[156:159], v[220:223], v[80:83]
	v_mfma_f32_16x16x32_bf16 v[124:127], v[160:163], v[178:181], v[124:127]
	v_mfma_f32_16x16x32_bf16 v[124:127], v[174:177], v[182:185], v[124:127]
	v_mfma_f32_16x16x32_bf16 v[108:111], v[160:163], v[186:189], v[108:111]
	v_mfma_f32_16x16x32_bf16 v[108:111], v[174:177], v[190:193], v[108:111]
	v_mfma_f32_16x16x32_bf16 v[92:95], v[160:163], v[202:205], v[92:95]
	v_mfma_f32_16x16x32_bf16 v[92:95], v[174:177], v[206:209], v[92:95]
	v_mfma_f32_16x16x32_bf16 v[76:79], v[160:163], v[216:219], v[76:79]
	v_mfma_f32_16x16x32_bf16 v[76:79], v[174:177], v[220:223], v[76:79]
	s_barrier
; #define PG8_MMA(ai, bj, At, Bt) do { __builtin_amdgcn_s_setprio(1); _Pragma("unroll") for (int m = 0; m < 4; ++m) _Pragma("unroll") for (int n = 0; n < 2; ++n) _Pragma("unroll") for (int k = 0; k < 2; ++k) \
;         acc[ai][bj][m][n] = __builtin_amdgcn_mfma_f32_16x16x32_bf16(Bt[n][k], At[m][k], acc[ai][bj][m][n], 0, 0, 0); __builtin_amdgcn_s_setprio(0); } while (0)
; #define PG8_WAIT_V(n) asm volatile("s_waitcnt vmcnt(" #n ")" ::: "memory")
; #define PG8_TRIP_HEAD(T) const int t = (T); const bool last = (t == nt - 2); \
;             const char* a1 = cA + (size_t)(t + 1) * kstep; \
;             const char* a2 = last ? nA : cA + (size_t)(t + 2) * kstep; const char* b2 = last ? nB : cB + (size_t)(t + 2) * kstep; \
;             const char* a3 = a2 + kstep; const char* b3 = b2 + kstep; \
;             if (last && has_next) S.a_ready(nxt);
; template <class Epi, class Sched, bool ALIGN_EPI = false, bool SP2 = false>
; __device__ __forceinline__ void gemm_phase(PG8_LAS unsigned char* lds, const Gemm g, const Sched& S, const Epi& E) {
;     ...
;         if constexpr (SP2) {
;             { PG8_TRIP_HEAD(0) PG8_TRIP_SP2(asm volatile("s_waitcnt vmcnt(%0)" :: "n"(8 + Epi::NST) : "memory"), PG8_MMAZ) }
;             for (int tt = 2; tt < nt; tt += 2) { PG8_TRIP_HEAD(tt) PG8_TRIP_SP2(PG8_WAIT_V(8), PG8_MMA) }
	s_mov_b32 m0, s46
	v_lshl_add_u64 v[224:225], v[194:195], 0, s[78:79]
	ds_read_b128 v[178:181], v200 offset:49152
	ds_read_b128 v[182:185], v200 offset:50176
	ds_read_b128 v[186:189], v200 offset:51200
	ds_read_b128 v[190:193], v200 offset:52224
	ds_read_b128 v[202:205], v200 offset:53248
	ds_read_b128 v[206:209], v200 offset:54272
	ds_read_b128 v[216:219], v200 offset:55296
	ds_read_b128 v[220:223], v200 offset:56320
	global_load_lds_dwordx4 v[224:225], off
	v_lshl_add_u64 v[224:225], v[194:195], 0, s[84:85]
	s_mov_b32 m0, s47
	s_nop 0
	global_load_lds_dwordx4 v[224:225], off
	v_lshl_add_u64 v[224:225], v[194:195], 0, s[56:57]
	s_mov_b32 m0, s48
	v_lshl_add_u64 v[194:195], v[194:195], 0, s[62:63]
	global_load_lds_dwordx4 v[224:225], off
	s_mov_b32 m0, s49
	s_nop 0
	global_load_lds_dwordx4 v[194:195], off
	v_lshl_add_u64 v[194:195], v[214:215], 0, s[78:79]
	s_mov_b32 m0, s38
	s_nop 0
	global_load_lds_dwordx4 v[194:195], off
	v_lshl_add_u64 v[194:195], v[214:215], 0, s[92:93]
	s_mov_b32 m0, s39
	s_nop 0
	global_load_lds_dwordx4 v[194:195], off
	s_waitcnt vmcnt(8)
	s_waitcnt lgkmcnt(0)
	s_barrier
	v_mfma_f32_16x16x32_bf16 v[56:59], v[136:139], v[178:181], v[56:59]
	v_mfma_f32_16x16x32_bf16 v[56:59], v[140:143], v[182:185], v[56:59]
	v_mfma_f32_16x16x32_bf16 v[40:43], v[136:139], v[186:189], v[40:43]
	v_mfma_f32_16x16x32_bf16 v[40:43], v[140:143], v[190:193], v[40:43]
	v_mfma_f32_16x16x32_bf16 v[24:27], v[136:139], v[202:205], v[24:27]
	v_mfma_f32_16x16x32_bf16 v[24:27], v[140:143], v[206:209], v[24:27]
	v_mfma_f32_16x16x32_bf16 v[8:11], v[136:139], v[216:219], v[8:11]
	v_mfma_f32_16x16x32_bf16 v[8:11], v[140:143], v[220:223], v[8:11]
	v_mfma_f32_16x16x32_bf16 v[52:55], v[144:147], v[178:181], v[52:55]
	v_mfma_f32_16x16x32_bf16 v[52:55], v[148:151], v[182:185], v[52:55]
	v_mfma_f32_16x16x32_bf16 v[36:39], v[144:147], v[186:189], v[36:39]
	v_mfma_f32_16x16x32_bf16 v[36:39], v[148:151], v[190:193], v[36:39]
	v_mfma_f32_16x16x32_bf16 v[20:23], v[144:147], v[202:205], v[20:23]
	v_mfma_f32_16x16x32_bf16 v[20:23], v[148:151], v[206:209], v[20:23]
	v_mfma_f32_16x16x32_bf16 v[4:7], v[144:147], v[216:219], v[4:7]
	v_mfma_f32_16x16x32_bf16 v[4:7], v[148:151], v[220:223], v[4:7]
	v_mfma_f32_16x16x32_bf16 v[64:67], v[152:155], v[178:181], v[64:67]
	v_mfma_f32_16x16x32_bf16 v[64:67], v[156:159], v[182:185], v[64:67]
	v_mfma_f32_16x16x32_bf16 v[48:51], v[152:155], v[186:189], v[48:51]
	v_mfma_f32_16x16x32_bf16 v[48:51], v[156:159], v[190:193], v[48:51]
	v_mfma_f32_16x16x32_bf16 v[32:35], v[152:155], v[202:205], v[32:35]
	v_mfma_f32_16x16x32_bf16 v[32:35], v[156:159], v[206:209], v[32:35]
	v_mfma_f32_16x16x32_bf16 v[16:19], v[152:155], v[216:219], v[16:19]
	v_mfma_f32_16x16x32_bf16 v[16:19], v[156:159], v[220:223], v[16:19]
	v_mfma_f32_16x16x32_bf16 v[60:63], v[160:163], v[178:181], v[60:63]
	v_mfma_f32_16x16x32_bf16 v[60:63], v[174:177], v[182:185], v[60:63]
	v_mfma_f32_16x16x32_bf16 v[44:47], v[160:163], v[186:189], v[44:47]
	v_mfma_f32_16x16x32_bf16 v[44:47], v[174:177], v[190:193], v[44:47]
	v_mfma_f32_16x16x32_bf16 v[28:31], v[160:163], v[202:205], v[28:31]
	v_mfma_f32_16x16x32_bf16 v[28:31], v[174:177], v[206:209], v[28:31]
	v_mfma_f32_16x16x32_bf16 v[12:15], v[160:163], v[216:219], v[12:15]
	v_mfma_f32_16x16x32_bf16 v[12:15], v[174:177], v[220:223], v[12:15]
	s_barrier
	s_add_i32 s14, s14, 2
	s_add_u32 s10, s10, 0x100
	s_addc_u32 s11, s11, 0
	s_add_u32 s12, s12, 0x100
	s_addc_u32 s13, s13, 0
	s_cmp_gt_u32 s14, 29
	s_cbranch_scc0 .LBB0_324
	s_and_b64 vcc, exec, s[18:19]
	s_cbranch_vccz .LBB0_327
	s_barrier

.LBB0_594:
	ds_read_b128 v[136:139], v116
	ds_read_b128 v[140:143], v116 offset:1024
	ds_read_b128 v[144:147], v116 offset:2048
	ds_read_b128 v[148:151], v116 offset:3072
	ds_read_b128 v[152:155], v117
	ds_read_b128 v[156:159], v117 offset:1024
	ds_read_b128 v[160:163], v117 offset:2048
	ds_read_b128 v[164:167], v117 offset:3072
	s_add_u32 s43, s20, 0xfff7c080
	s_addc_u32 s44, s21, -1
	s_cmp_eq_u32 s15, 28
	s_cselect_b32 s45, s17, s44
	s_cselect_b32 s44, s16, s43
	s_cselect_b32 s47, s4, s9
	s_cselect_b32 s46, s5, s8
	s_mov_b32 m0, s33
	v_lshl_add_u64 v[192:193], s[20:21], 0, v[200:201]
	ds_read_b128 v[168:171], v221
	ds_read_b128 v[172:175], v221 offset:1024
	ds_read_b128 v[176:179], v221 offset:2048
	ds_read_b128 v[180:183], v221 offset:3072
	ds_read_b128 v[184:187], v221 offset:4096
	ds_read_b128 v[188:191], v221 offset:5120
	ds_read_b128 v[202:205], v221 offset:6144
	ds_read_b128 v[206:209], v221 offset:7168
	global_load_lds_dwordx4 v[192:193], off
	v_lshl_add_u64 v[192:193], v[192:193], 0, s[96:97]
	s_mov_b32 m0, s34
	s_nop 0
	global_load_lds_dwordx4 v[192:193], off
	s_waitcnt vmcnt(8)
	s_waitcnt lgkmcnt(0)
	s_barrier
	v_mfma_f32_16x16x32_bf16 v[130:133], v[136:139], v[168:171], v[130:133]
	v_mfma_f32_16x16x32_bf16 v[130:133], v[140:143], v[172:175], v[130:133]
	v_mfma_f32_16x16x32_bf16 v[112:115], v[136:139], v[176:179], v[112:115]
	v_mfma_f32_16x16x32_bf16 v[112:115], v[140:143], v[180:183], v[112:115]
	v_mfma_f32_16x16x32_bf16 v[96:99], v[136:139], v[184:187], v[96:99]
	v_mfma_f32_16x16x32_bf16 v[96:99], v[140:143], v[188:191], v[96:99]
	v_mfma_f32_16x16x32_bf16 v[80:83], v[136:139], v[202:205], v[80:83]
	v_mfma_f32_16x16x32_bf16 v[80:83], v[140:143], v[206:209], v[80:83]
	v_mfma_f32_16x16x32_bf16 v[126:129], v[144:147], v[168:171], v[126:129]
	v_mfma_f32_16x16x32_bf16 v[126:129], v[148:151], v[172:175], v[126:129]
	v_mfma_f32_16x16x32_bf16 v[108:111], v[144:147], v[176:179], v[108:111]
	v_mfma_f32_16x16x32_bf16 v[108:111], v[148:151], v[180:183], v[108:111]
	v_mfma_f32_16x16x32_bf16 v[92:95], v[144:147], v[184:187], v[92:95]
	v_mfma_f32_16x16x32_bf16 v[92:95], v[148:151], v[188:191], v[92:95]
	v_mfma_f32_16x16x32_bf16 v[76:79], v[144:147], v[202:205], v[76:79]
	v_mfma_f32_16x16x32_bf16 v[76:79], v[148:151], v[206:209], v[76:79]
	v_mfma_f32_16x16x32_bf16 v[122:125], v[152:155], v[168:171], v[122:125]
	v_mfma_f32_16x16x32_bf16 v[122:125], v[156:159], v[172:175], v[122:125]
	v_mfma_f32_16x16x32_bf16 v[104:107], v[152:155], v[176:179], v[104:107]
	v_mfma_f32_16x16x32_bf16 v[104:107], v[156:159], v[180:183], v[104:107]
	v_mfma_f32_16x16x32_bf16 v[88:91], v[152:155], v[184:187], v[88:91]
	v_mfma_f32_16x16x32_bf16 v[88:91], v[156:159], v[188:191], v[88:91]
	v_mfma_f32_16x16x32_bf16 v[72:75], v[152:155], v[202:205], v[72:75]
	v_mfma_f32_16x16x32_bf16 v[72:75], v[156:159], v[206:209], v[72:75]
	v_mfma_f32_16x16x32_bf16 v[118:121], v[160:163], v[168:171], v[118:121]
	v_mfma_f32_16x16x32_bf16 v[118:121], v[164:167], v[172:175], v[118:121]
	v_mfma_f32_16x16x32_bf16 v[100:103], v[160:163], v[176:179], v[100:103]
	v_mfma_f32_16x16x32_bf16 v[100:103], v[164:167], v[180:183], v[100:103]
	v_mfma_f32_16x16x32_bf16 v[84:87], v[160:163], v[184:187], v[84:87]
	v_mfma_f32_16x16x32_bf16 v[84:87], v[164:167], v[188:191], v[84:87]
	v_mfma_f32_16x16x32_bf16 v[68:71], v[160:163], v[202:205], v[68:71]
	v_mfma_f32_16x16x32_bf16 v[68:71], v[164:167], v[206:209], v[68:71]
	s_barrier
	s_mov_b32 m0, s35
	v_lshl_add_u64 v[192:193], s[46:47], 0, v[194:195]
	ds_read_b128 v[168:171], v221 offset:16384
	ds_read_b128 v[172:175], v221 offset:17408
	ds_read_b128 v[176:179], v221 offset:18432
	ds_read_b128 v[180:183], v221 offset:19456
	ds_read_b128 v[184:187], v221 offset:20480
	ds_read_b128 v[188:191], v221 offset:21504
	ds_read_b128 v[202:205], v221 offset:22528
	ds_read_b128 v[206:209], v221 offset:23552
	global_load_lds_dwordx4 v[192:193], off
	v_lshl_add_u64 v[214:215], v[192:193], 0, s[90:91]
	s_mov_b32 m0, s36
	s_nop 0
	global_load_lds_dwordx4 v[214:215], off
	v_lshl_add_u64 v[214:215], v[192:193], 0, s[48:49]
	s_mov_b32 m0, s37
	s_nop 0
	global_load_lds_dwordx4 v[214:215], off
	v_lshl_add_u64 v[214:215], v[192:193], 0, s[52:53]
	s_mov_b32 m0, s38
	s_nop 0
	global_load_lds_dwordx4 v[214:215], off
	v_lshl_add_u64 v[214:215], s[44:45], 0, v[196:197]
	s_mov_b32 m0, s23
	v_lshl_add_u64 v[216:217], v[214:215], 0, s[96:97]
	global_load_lds_dwordx4 v[214:215], off
	s_mov_b32 m0, s24
	s_nop 0
	global_load_lds_dwordx4 v[216:217], off
	s_waitcnt vmcnt(8)
	s_waitcnt lgkmcnt(0)
	s_barrier
	v_mfma_f32_16x16x32_bf16 v[64:67], v[136:139], v[168:171], v[64:67]
	v_mfma_f32_16x16x32_bf16 v[64:67], v[140:143], v[172:175], v[64:67]
	v_mfma_f32_16x16x32_bf16 v[48:51], v[136:139], v[176:179], v[48:51]
	v_mfma_f32_16x16x32_bf16 v[48:51], v[140:143], v[180:183], v[48:51]
	v_mfma_f32_16x16x32_bf16 v[32:35], v[136:139], v[184:187], v[32:35]
	v_mfma_f32_16x16x32_bf16 v[32:35], v[140:143], v[188:191], v[32:35]
	v_mfma_f32_16x16x32_bf16 v[16:19], v[136:139], v[202:205], v[16:19]
	v_mfma_f32_16x16x32_bf16 v[16:19], v[140:143], v[206:209], v[16:19]
	v_mfma_f32_16x16x32_bf16 v[60:63], v[144:147], v[168:171], v[60:63]
	v_mfma_f32_16x16x32_bf16 v[60:63], v[148:151], v[172:175], v[60:63]
	v_mfma_f32_16x16x32_bf16 v[44:47], v[144:147], v[176:179], v[44:47]
	v_mfma_f32_16x16x32_bf16 v[44:47], v[148:151], v[180:183], v[44:47]
	v_mfma_f32_16x16x32_bf16 v[28:31], v[144:147], v[184:187], v[28:31]
	v_mfma_f32_16x16x32_bf16 v[28:31], v[148:151], v[188:191], v[28:31]
	v_mfma_f32_16x16x32_bf16 v[12:15], v[144:147], v[202:205], v[12:15]
	v_mfma_f32_16x16x32_bf16 v[12:15], v[148:151], v[206:209], v[12:15]
	v_mfma_f32_16x16x32_bf16 v[56:59], v[152:155], v[168:171], v[56:59]
	v_mfma_f32_16x16x32_bf16 v[56:59], v[156:159], v[172:175], v[56:59]
	v_mfma_f32_16x16x32_bf16 v[40:43], v[152:155], v[176:179], v[40:43]
	v_mfma_f32_16x16x32_bf16 v[40:43], v[156:159], v[180:183], v[40:43]
	v_mfma_f32_16x16x32_bf16 v[24:27], v[152:155], v[184:187], v[24:27]
	v_mfma_f32_16x16x32_bf16 v[24:27], v[156:159], v[188:191], v[24:27]
	v_mfma_f32_16x16x32_bf16 v[8:11], v[152:155], v[202:205], v[8:11]
	v_mfma_f32_16x16x32_bf16 v[8:11], v[156:159], v[206:209], v[8:11]
	v_mfma_f32_16x16x32_bf16 v[52:55], v[160:163], v[168:171], v[52:55]
	v_mfma_f32_16x16x32_bf16 v[52:55], v[164:167], v[172:175], v[52:55]
	v_mfma_f32_16x16x32_bf16 v[36:39], v[160:163], v[176:179], v[36:39]
	v_mfma_f32_16x16x32_bf16 v[36:39], v[164:167], v[180:183], v[36:39]
	v_mfma_f32_16x16x32_bf16 v[20:23], v[160:163], v[184:187], v[20:23]
	v_mfma_f32_16x16x32_bf16 v[20:23], v[164:167], v[188:191], v[20:23]
	v_mfma_f32_16x16x32_bf16 v[4:7], v[160:163], v[202:205], v[4:7]
	v_mfma_f32_16x16x32_bf16 v[4:7], v[164:167], v[206:209], v[4:7]
	s_barrier
; #define PG8_MMA(ai, bj, At, Bt) do { __builtin_amdgcn_s_setprio(1); _Pragma("unroll") for (int m = 0; m < 4; ++m) _Pragma("unroll") for (int n = 0; n < 2; ++n) _Pragma("unroll") for (int k = 0; k < 2; ++k) \
;         acc[ai][bj][m][n] = __builtin_amdgcn_mfma_f32_16x16x32_bf16(Bt[n][k], At[m][k], acc[ai][bj][m][n], 0, 0, 0); __builtin_amdgcn_s_setprio(0); } while (0)
; #define PG8_WAIT_V(n) asm volatile("s_waitcnt vmcnt(" #n ")" ::: "memory")
; #define PG8_TRIP_HEAD(T) const int t = (T); const bool last = (t == nt - 2); \
;             const char* a1 = cA + (size_t)(t + 1) * kstep; \
;             const char* a2 = last ? nA : cA + (size_t)(t + 2) * kstep; const char* b2 = last ? nB : cB + (size_t)(t + 2) * kstep; \
;             const char* a3 = a2 + kstep; const char* b3 = b2 + kstep; \
;             if (last && has_next) S.a_ready(nxt);
; template <class Epi, class Sched, bool ALIGN_EPI = false, bool SP2 = false>
; __device__ __forceinline__ void gemm_phase(PG8_LAS unsigned char* lds, const Gemm g, const Sched& S, const Epi& E) {
;     ...
;         if constexpr (SP2) {
;             { PG8_TRIP_HEAD(0) PG8_TRIP_SP2(asm volatile("s_waitcnt vmcnt(%0)" :: "n"(8 + Epi::NST) : "memory"), PG8_MMAZ) }
;             for (int tt = 2; tt < nt; tt += 2) { PG8_TRIP_HEAD(tt) PG8_TRIP_SP2(PG8_WAIT_V(8), PG8_MMA) }
	ds_read_b128 v[136:139], v134
	ds_read_b128 v[140:143], v134 offset:1024
	ds_read_b128 v[144:147], v134 offset:2048
	ds_read_b128 v[148:151], v134 offset:3072
	ds_read_b128 v[152:155], v135
	ds_read_b128 v[156:159], v135 offset:1024
	ds_read_b128 v[160:163], v135 offset:2048
	ds_read_b128 v[164:167], v135 offset:3072
	s_mov_b32 m0, s25
	v_lshl_add_u64 v[216:217], v[214:215], 0, s[82:83]
	ds_read_b128 v[168:171], v221 offset:32768
	ds_read_b128 v[172:175], v221 offset:33792
	ds_read_b128 v[176:179], v221 offset:34816
	ds_read_b128 v[180:183], v221 offset:35840
	ds_read_b128 v[184:187], v221 offset:36864
	ds_read_b128 v[188:191], v221 offset:37888
	ds_read_b128 v[202:205], v221 offset:38912
	ds_read_b128 v[206:209], v221 offset:39936
	global_load_lds_dwordx4 v[216:217], off
	v_lshl_add_u64 v[216:217], v[214:215], 0, s[56:57]
	s_mov_b32 m0, s26
	s_nop 0
	global_load_lds_dwordx4 v[216:217], off
	s_waitcnt vmcnt(8)
	s_waitcnt lgkmcnt(0)
	s_barrier
	v_mfma_f32_16x16x32_bf16 v[130:133], v[136:139], v[168:171], v[130:133]
	v_mfma_f32_16x16x32_bf16 v[130:133], v[140:143], v[172:175], v[130:133]
	v_mfma_f32_16x16x32_bf16 v[112:115], v[136:139], v[176:179], v[112:115]
	v_mfma_f32_16x16x32_bf16 v[112:115], v[140:143], v[180:183], v[112:115]
	v_mfma_f32_16x16x32_bf16 v[96:99], v[136:139], v[184:187], v[96:99]
	v_mfma_f32_16x16x32_bf16 v[96:99], v[140:143], v[188:191], v[96:99]
	v_mfma_f32_16x16x32_bf16 v[80:83], v[136:139], v[202:205], v[80:83]
	v_mfma_f32_16x16x32_bf16 v[80:83], v[140:143], v[206:209], v[80:83]
	v_mfma_f32_16x16x32_bf16 v[126:129], v[144:147], v[168:171], v[126:129]
	v_mfma_f32_16x16x32_bf16 v[126:129], v[148:151], v[172:175], v[126:129]
	v_mfma_f32_16x16x32_bf16 v[108:111], v[144:147], v[176:179], v[108:111]
	v_mfma_f32_16x16x32_bf16 v[108:111], v[148:151], v[180:183], v[108:111]
	v_mfma_f32_16x16x32_bf16 v[92:95], v[144:147], v[184:187], v[92:95]
	v_mfma_f32_16x16x32_bf16 v[92:95], v[148:151], v[188:191], v[92:95]
	v_mfma_f32_16x16x32_bf16 v[76:79], v[144:147], v[202:205], v[76:79]
	v_mfma_f32_16x16x32_bf16 v[76:79], v[148:151], v[206:209], v[76:79]
	v_mfma_f32_16x16x32_bf16 v[122:125], v[152:155], v[168:171], v[122:125]
	v_mfma_f32_16x16x32_bf16 v[122:125], v[156:159], v[172:175], v[122:125]
	v_mfma_f32_16x16x32_bf16 v[104:107], v[152:155], v[176:179], v[104:107]
	v_mfma_f32_16x16x32_bf16 v[104:107], v[156:159], v[180:183], v[104:107]
	v_mfma_f32_16x16x32_bf16 v[88:91], v[152:155], v[184:187], v[88:91]
	v_mfma_f32_16x16x32_bf16 v[88:91], v[156:159], v[188:191], v[88:91]
	v_mfma_f32_16x16x32_bf16 v[72:75], v[152:155], v[202:205], v[72:75]
	v_mfma_f32_16x16x32_bf16 v[72:75], v[156:159], v[206:209], v[72:75]
	v_mfma_f32_16x16x32_bf16 v[118:121], v[160:163], v[168:171], v[118:121]
	v_mfma_f32_16x16x32_bf16 v[118:121], v[164:167], v[172:175], v[118:121]
	v_mfma_f32_16x16x32_bf16 v[100:103], v[160:163], v[176:179], v[100:103]
	v_mfma_f32_16x16x32_bf16 v[100:103], v[164:167], v[180:183], v[100:103]
	v_mfma_f32_16x16x32_bf16 v[84:87], v[160:163], v[184:187], v[84:87]
	v_mfma_f32_16x16x32_bf16 v[84:87], v[164:167], v[188:191], v[84:87]
	v_mfma_f32_16x16x32_bf16 v[68:71], v[160:163], v[202:205], v[68:71]
	v_mfma_f32_16x16x32_bf16 v[68:71], v[164:167], v[206:209], v[68:71]
	s_barrier
	s_mov_b32 m0, s39
	v_lshl_add_u64 v[216:217], v[192:193], 0, s[78:79]
	ds_read_b128 v[168:171], v221 offset:49152
	ds_read_b128 v[172:175], v221 offset:50176
	ds_read_b128 v[176:179], v221 offset:51200
	ds_read_b128 v[180:183], v221 offset:52224
	ds_read_b128 v[184:187], v221 offset:53248
	ds_read_b128 v[188:191], v221 offset:54272
	ds_read_b128 v[202:205], v221 offset:55296
	ds_read_b128 v[206:209], v221 offset:56320
	global_load_lds_dwordx4 v[216:217], off
	v_lshl_add_u64 v[216:217], v[192:193], 0, s[84:85]
	s_mov_b32 m0, s40
	s_nop 0
	global_load_lds_dwordx4 v[216:217], off
	v_lshl_add_u64 v[216:217], v[192:193], 0, s[50:51]
	s_mov_b32 m0, s41
	v_lshl_add_u64 v[192:193], v[192:193], 0, s[54:55]
	global_load_lds_dwordx4 v[216:217], off
	s_mov_b32 m0, s42
	s_nop 0
	global_load_lds_dwordx4 v[192:193], off
	v_lshl_add_u64 v[192:193], v[214:215], 0, s[78:79]
	s_mov_b32 m0, s27
	s_nop 0
	global_load_lds_dwordx4 v[192:193], off
	v_lshl_add_u64 v[192:193], v[214:215], 0, s[92:93]
	s_mov_b32 m0, s28
	s_nop 0
	global_load_lds_dwordx4 v[192:193], off
	s_waitcnt vmcnt(8)
	s_waitcnt lgkmcnt(0)
	s_barrier
	v_mfma_f32_16x16x32_bf16 v[64:67], v[136:139], v[168:171], v[64:67]
	v_mfma_f32_16x16x32_bf16 v[64:67], v[140:143], v[172:175], v[64:67]
	v_mfma_f32_16x16x32_bf16 v[48:51], v[136:139], v[176:179], v[48:51]
	v_mfma_f32_16x16x32_bf16 v[48:51], v[140:143], v[180:183], v[48:51]
	v_mfma_f32_16x16x32_bf16 v[32:35], v[136:139], v[184:187], v[32:35]
	v_mfma_f32_16x16x32_bf16 v[32:35], v[140:143], v[188:191], v[32:35]
	v_mfma_f32_16x16x32_bf16 v[16:19], v[136:139], v[202:205], v[16:19]
	v_mfma_f32_16x16x32_bf16 v[16:19], v[140:143], v[206:209], v[16:19]
	v_mfma_f32_16x16x32_bf16 v[60:63], v[144:147], v[168:171], v[60:63]
	v_mfma_f32_16x16x32_bf16 v[60:63], v[148:151], v[172:175], v[60:63]
	v_mfma_f32_16x16x32_bf16 v[44:47], v[144:147], v[176:179], v[44:47]
	v_mfma_f32_16x16x32_bf16 v[44:47], v[148:151], v[180:183], v[44:47]
	v_mfma_f32_16x16x32_bf16 v[28:31], v[144:147], v[184:187], v[28:31]
	v_mfma_f32_16x16x32_bf16 v[28:31], v[148:151], v[188:191], v[28:31]
	v_mfma_f32_16x16x32_bf16 v[12:15], v[144:147], v[202:205], v[12:15]
	v_mfma_f32_16x16x32_bf16 v[12:15], v[148:151], v[206:209], v[12:15]
	v_mfma_f32_16x16x32_bf16 v[56:59], v[152:155], v[168:171], v[56:59]
	v_mfma_f32_16x16x32_bf16 v[56:59], v[156:159], v[172:175], v[56:59]
	v_mfma_f32_16x16x32_bf16 v[40:43], v[152:155], v[176:179], v[40:43]
	v_mfma_f32_16x16x32_bf16 v[40:43], v[156:159], v[180:183], v[40:43]
	v_mfma_f32_16x16x32_bf16 v[24:27], v[152:155], v[184:187], v[24:27]
	v_mfma_f32_16x16x32_bf16 v[24:27], v[156:159], v[188:191], v[24:27]
	v_mfma_f32_16x16x32_bf16 v[8:11], v[152:155], v[202:205], v[8:11]
	v_mfma_f32_16x16x32_bf16 v[8:11], v[156:159], v[206:209], v[8:11]
	v_mfma_f32_16x16x32_bf16 v[52:55], v[160:163], v[168:171], v[52:55]
	v_mfma_f32_16x16x32_bf16 v[52:55], v[164:167], v[172:175], v[52:55]
	v_mfma_f32_16x16x32_bf16 v[36:39], v[160:163], v[176:179], v[36:39]
	v_mfma_f32_16x16x32_bf16 v[36:39], v[164:167], v[180:183], v[36:39]
	v_mfma_f32_16x16x32_bf16 v[20:23], v[160:163], v[184:187], v[20:23]
	v_mfma_f32_16x16x32_bf16 v[20:23], v[164:167], v[188:191], v[20:23]
	v_mfma_f32_16x16x32_bf16 v[4:7], v[160:163], v[202:205], v[4:7]
	v_mfma_f32_16x16x32_bf16 v[4:7], v[164:167], v[206:209], v[4:7]
	s_barrier
	s_add_i32 s15, s15, 2
	s_add_u32 s20, s20, 0x100
	s_addc_u32 s21, s21, 0
	s_add_u32 s8, s8, 0x100
	s_addc_u32 s9, s9, 0
	s_cmp_gt_u32 s15, 29
	s_cbranch_scc0 .LBB0_594
	s_and_b64 vcc, exec, s[12:13]
	s_cbranch_vccz .LBB0_597
	s_barrier

.LBB0_700:
	ds_read_b128 v[120:123], v116
	ds_read_b128 v[132:135], v116 offset:1024
	ds_read_b128 v[144:147], v116 offset:2048
	ds_read_b128 v[148:151], v116 offset:3072
	ds_read_b128 v[152:155], v117
	ds_read_b128 v[156:159], v117 offset:1024
	ds_read_b128 v[166:169], v117 offset:2048
	ds_read_b128 v[170:173], v117 offset:3072
	s_add_u32 s27, s10, 0xfff7c080
	s_addc_u32 s47, s11, -1
	s_cmp_eq_u32 s26, 28
	s_cselect_b32 s49, s21, s47
	s_cselect_b32 s48, s20, s27
	s_cselect_b32 s51, s3, s25
	s_cselect_b32 s50, s4, s24
	s_mov_b32 m0, s5
	v_lshl_add_u64 v[208:209], s[10:11], 0, v[164:165]
	ds_read_b128 v[180:183], v178
	ds_read_b128 v[184:187], v178 offset:1024
	ds_read_b128 v[188:191], v178 offset:2048
	ds_read_b128 v[192:195], v178 offset:3072
	ds_read_b128 v[196:199], v178 offset:4096
	ds_read_b128 v[200:203], v178 offset:5120
	ds_read_b128 v[204:207], v178 offset:6144
	ds_read_b128 v[214:217], v178 offset:7168
	global_load_lds_dwordx4 v[208:209], off
	v_lshl_add_u64 v[208:209], v[208:209], 0, s[96:97]
	s_mov_b32 m0, s19
	s_nop 0
	global_load_lds_dwordx4 v[208:209], off
	s_waitcnt vmcnt(8)
	s_waitcnt lgkmcnt(0)
	s_barrier
	v_mfma_f32_16x16x32_bf16 v[140:143], v[120:123], v[180:183], v[140:143]
	v_mfma_f32_16x16x32_bf16 v[140:143], v[132:135], v[184:187], v[140:143]
	v_mfma_f32_16x16x32_bf16 v[112:115], v[120:123], v[188:191], v[112:115]
	v_mfma_f32_16x16x32_bf16 v[112:115], v[132:135], v[192:195], v[112:115]
	v_mfma_f32_16x16x32_bf16 v[96:99], v[120:123], v[196:199], v[96:99]
	v_mfma_f32_16x16x32_bf16 v[96:99], v[132:135], v[200:203], v[96:99]
	v_mfma_f32_16x16x32_bf16 v[80:83], v[120:123], v[204:207], v[80:83]
	v_mfma_f32_16x16x32_bf16 v[80:83], v[132:135], v[214:217], v[80:83]
	v_mfma_f32_16x16x32_bf16 v[136:139], v[144:147], v[180:183], v[136:139]
	v_mfma_f32_16x16x32_bf16 v[136:139], v[148:151], v[184:187], v[136:139]
	v_mfma_f32_16x16x32_bf16 v[108:111], v[144:147], v[188:191], v[108:111]
	v_mfma_f32_16x16x32_bf16 v[108:111], v[148:151], v[192:195], v[108:111]
	v_mfma_f32_16x16x32_bf16 v[92:95], v[144:147], v[196:199], v[92:95]
	v_mfma_f32_16x16x32_bf16 v[92:95], v[148:151], v[200:203], v[92:95]
	v_mfma_f32_16x16x32_bf16 v[76:79], v[144:147], v[204:207], v[76:79]
	v_mfma_f32_16x16x32_bf16 v[76:79], v[148:151], v[214:217], v[76:79]
	v_mfma_f32_16x16x32_bf16 v[128:131], v[152:155], v[180:183], v[128:131]
	v_mfma_f32_16x16x32_bf16 v[128:131], v[156:159], v[184:187], v[128:131]
	v_mfma_f32_16x16x32_bf16 v[104:107], v[152:155], v[188:191], v[104:107]
	v_mfma_f32_16x16x32_bf16 v[104:107], v[156:159], v[192:195], v[104:107]
	v_mfma_f32_16x16x32_bf16 v[88:91], v[152:155], v[196:199], v[88:91]
	v_mfma_f32_16x16x32_bf16 v[88:91], v[156:159], v[200:203], v[88:91]
	v_mfma_f32_16x16x32_bf16 v[72:75], v[152:155], v[204:207], v[72:75]
	v_mfma_f32_16x16x32_bf16 v[72:75], v[156:159], v[214:217], v[72:75]
	v_mfma_f32_16x16x32_bf16 v[124:127], v[166:169], v[180:183], v[124:127]
	v_mfma_f32_16x16x32_bf16 v[124:127], v[170:173], v[184:187], v[124:127]
	v_mfma_f32_16x16x32_bf16 v[100:103], v[166:169], v[188:191], v[100:103]
	v_mfma_f32_16x16x32_bf16 v[100:103], v[170:173], v[192:195], v[100:103]
	v_mfma_f32_16x16x32_bf16 v[84:87], v[166:169], v[196:199], v[84:87]
	v_mfma_f32_16x16x32_bf16 v[84:87], v[170:173], v[200:203], v[84:87]
	v_mfma_f32_16x16x32_bf16 v[68:71], v[166:169], v[204:207], v[68:71]
	v_mfma_f32_16x16x32_bf16 v[68:71], v[170:173], v[214:217], v[68:71]
	s_barrier
	s_mov_b32 m0, s33
	v_lshl_add_u64 v[208:209], s[50:51], 0, v[160:161]
	ds_read_b128 v[180:183], v178 offset:16384
	ds_read_b128 v[184:187], v178 offset:17408
	ds_read_b128 v[188:191], v178 offset:18432
	ds_read_b128 v[192:195], v178 offset:19456
	ds_read_b128 v[196:199], v178 offset:20480
	ds_read_b128 v[200:203], v178 offset:21504
	ds_read_b128 v[204:207], v178 offset:22528
	ds_read_b128 v[214:217], v178 offset:23552
	global_load_lds_dwordx4 v[208:209], off
	v_lshl_add_u64 v[218:219], v[208:209], 0, s[90:91]
	s_mov_b32 m0, s40
	s_nop 0
	global_load_lds_dwordx4 v[218:219], off
	v_lshl_add_u64 v[218:219], v[208:209], 0, s[52:53]
	s_mov_b32 m0, s41
	s_nop 0
	global_load_lds_dwordx4 v[218:219], off
	v_lshl_add_u64 v[218:219], v[208:209], 0, s[56:57]
	s_mov_b32 m0, s42
	s_nop 0
	global_load_lds_dwordx4 v[218:219], off
	v_lshl_add_u64 v[218:219], s[48:49], 0, v[162:163]
	s_mov_b32 m0, s29
	v_lshl_add_u64 v[220:221], v[218:219], 0, s[96:97]
	global_load_lds_dwordx4 v[218:219], off
	s_mov_b32 m0, s30
	s_nop 0
	global_load_lds_dwordx4 v[220:221], off
	s_waitcnt vmcnt(8)
	s_waitcnt lgkmcnt(0)
	s_barrier
	v_mfma_f32_16x16x32_bf16 v[56:59], v[120:123], v[180:183], v[56:59]
	v_mfma_f32_16x16x32_bf16 v[56:59], v[132:135], v[184:187], v[56:59]
	v_mfma_f32_16x16x32_bf16 v[48:51], v[120:123], v[188:191], v[48:51]
	v_mfma_f32_16x16x32_bf16 v[48:51], v[132:135], v[192:195], v[48:51]
	v_mfma_f32_16x16x32_bf16 v[32:35], v[120:123], v[196:199], v[32:35]
	v_mfma_f32_16x16x32_bf16 v[32:35], v[132:135], v[200:203], v[32:35]
	v_mfma_f32_16x16x32_bf16 v[16:19], v[120:123], v[204:207], v[16:19]
	v_mfma_f32_16x16x32_bf16 v[16:19], v[132:135], v[214:217], v[16:19]
	v_mfma_f32_16x16x32_bf16 v[52:55], v[144:147], v[180:183], v[52:55]
	v_mfma_f32_16x16x32_bf16 v[52:55], v[148:151], v[184:187], v[52:55]
	v_mfma_f32_16x16x32_bf16 v[44:47], v[144:147], v[188:191], v[44:47]
	v_mfma_f32_16x16x32_bf16 v[44:47], v[148:151], v[192:195], v[44:47]
	v_mfma_f32_16x16x32_bf16 v[28:31], v[144:147], v[196:199], v[28:31]
	v_mfma_f32_16x16x32_bf16 v[28:31], v[148:151], v[200:203], v[28:31]
	v_mfma_f32_16x16x32_bf16 v[12:15], v[144:147], v[204:207], v[12:15]
	v_mfma_f32_16x16x32_bf16 v[12:15], v[148:151], v[214:217], v[12:15]
	v_mfma_f32_16x16x32_bf16 v[64:67], v[152:155], v[180:183], v[64:67]
	v_mfma_f32_16x16x32_bf16 v[64:67], v[156:159], v[184:187], v[64:67]
	v_mfma_f32_16x16x32_bf16 v[40:43], v[152:155], v[188:191], v[40:43]
	v_mfma_f32_16x16x32_bf16 v[40:43], v[156:159], v[192:195], v[40:43]
	v_mfma_f32_16x16x32_bf16 v[24:27], v[152:155], v[196:199], v[24:27]
	v_mfma_f32_16x16x32_bf16 v[24:27], v[156:159], v[200:203], v[24:27]
	v_mfma_f32_16x16x32_bf16 v[8:11], v[152:155], v[204:207], v[8:11]
	v_mfma_f32_16x16x32_bf16 v[8:11], v[156:159], v[214:217], v[8:11]
	v_mfma_f32_16x16x32_bf16 v[60:63], v[166:169], v[180:183], v[60:63]
	v_mfma_f32_16x16x32_bf16 v[60:63], v[170:173], v[184:187], v[60:63]
	v_mfma_f32_16x16x32_bf16 v[36:39], v[166:169], v[188:191], v[36:39]
	v_mfma_f32_16x16x32_bf16 v[36:39], v[170:173], v[192:195], v[36:39]
	v_mfma_f32_16x16x32_bf16 v[20:23], v[166:169], v[196:199], v[20:23]
	v_mfma_f32_16x16x32_bf16 v[20:23], v[170:173], v[200:203], v[20:23]
	v_mfma_f32_16x16x32_bf16 v[4:7], v[166:169], v[204:207], v[4:7]
	v_mfma_f32_16x16x32_bf16 v[4:7], v[170:173], v[214:217], v[4:7]
	s_barrier
	ds_read_b128 v[120:123], v118
	ds_read_b128 v[132:135], v118 offset:1024
	ds_read_b128 v[144:147], v118 offset:2048
	ds_read_b128 v[148:151], v118 offset:3072
	ds_read_b128 v[152:155], v119
	ds_read_b128 v[156:159], v119 offset:1024
	ds_read_b128 v[166:169], v119 offset:2048
	ds_read_b128 v[170:173], v119 offset:3072
	s_mov_b32 m0, s31
	v_lshl_add_u64 v[220:221], v[218:219], 0, s[82:83]
	ds_read_b128 v[180:183], v178 offset:32768
	ds_read_b128 v[184:187], v178 offset:33792
	ds_read_b128 v[188:191], v178 offset:34816
	ds_read_b128 v[192:195], v178 offset:35840
	ds_read_b128 v[196:199], v178 offset:36864
	ds_read_b128 v[200:203], v178 offset:37888
	ds_read_b128 v[204:207], v178 offset:38912
	ds_read_b128 v[214:217], v178 offset:39936
	global_load_lds_dwordx4 v[220:221], off
	v_lshl_add_u64 v[220:221], v[218:219], 0, s[62:63]
	s_mov_b32 m0, s34
	s_nop 0
	global_load_lds_dwordx4 v[220:221], off
	s_waitcnt vmcnt(8)
	s_waitcnt lgkmcnt(0)
	s_barrier
	v_mfma_f32_16x16x32_bf16 v[140:143], v[120:123], v[180:183], v[140:143]
	v_mfma_f32_16x16x32_bf16 v[140:143], v[132:135], v[184:187], v[140:143]
	v_mfma_f32_16x16x32_bf16 v[112:115], v[120:123], v[188:191], v[112:115]
	v_mfma_f32_16x16x32_bf16 v[112:115], v[132:135], v[192:195], v[112:115]
	v_mfma_f32_16x16x32_bf16 v[96:99], v[120:123], v[196:199], v[96:99]
	v_mfma_f32_16x16x32_bf16 v[96:99], v[132:135], v[200:203], v[96:99]
	v_mfma_f32_16x16x32_bf16 v[80:83], v[120:123], v[204:207], v[80:83]
	v_mfma_f32_16x16x32_bf16 v[80:83], v[132:135], v[214:217], v[80:83]
	v_mfma_f32_16x16x32_bf16 v[136:139], v[144:147], v[180:183], v[136:139]
	v_mfma_f32_16x16x32_bf16 v[136:139], v[148:151], v[184:187], v[136:139]
	v_mfma_f32_16x16x32_bf16 v[108:111], v[144:147], v[188:191], v[108:111]
	v_mfma_f32_16x16x32_bf16 v[108:111], v[148:151], v[192:195], v[108:111]
	v_mfma_f32_16x16x32_bf16 v[92:95], v[144:147], v[196:199], v[92:95]
	v_mfma_f32_16x16x32_bf16 v[92:95], v[148:151], v[200:203], v[92:95]
	v_mfma_f32_16x16x32_bf16 v[76:79], v[144:147], v[204:207], v[76:79]
	v_mfma_f32_16x16x32_bf16 v[76:79], v[148:151], v[214:217], v[76:79]
	v_mfma_f32_16x16x32_bf16 v[128:131], v[152:155], v[180:183], v[128:131]
	v_mfma_f32_16x16x32_bf16 v[128:131], v[156:159], v[184:187], v[128:131]
	v_mfma_f32_16x16x32_bf16 v[104:107], v[152:155], v[188:191], v[104:107]
	v_mfma_f32_16x16x32_bf16 v[104:107], v[156:159], v[192:195], v[104:107]
	v_mfma_f32_16x16x32_bf16 v[88:91], v[152:155], v[196:199], v[88:91]
	v_mfma_f32_16x16x32_bf16 v[88:91], v[156:159], v[200:203], v[88:91]
	v_mfma_f32_16x16x32_bf16 v[72:75], v[152:155], v[204:207], v[72:75]
	v_mfma_f32_16x16x32_bf16 v[72:75], v[156:159], v[214:217], v[72:75]
	v_mfma_f32_16x16x32_bf16 v[124:127], v[166:169], v[180:183], v[124:127]
	v_mfma_f32_16x16x32_bf16 v[124:127], v[170:173], v[184:187], v[124:127]
	v_mfma_f32_16x16x32_bf16 v[100:103], v[166:169], v[188:191], v[100:103]
	v_mfma_f32_16x16x32_bf16 v[100:103], v[170:173], v[192:195], v[100:103]
	v_mfma_f32_16x16x32_bf16 v[84:87], v[166:169], v[196:199], v[84:87]
	v_mfma_f32_16x16x32_bf16 v[84:87], v[170:173], v[200:203], v[84:87]
	v_mfma_f32_16x16x32_bf16 v[68:71], v[166:169], v[204:207], v[68:71]
	v_mfma_f32_16x16x32_bf16 v[68:71], v[170:173], v[214:217], v[68:71]
	s_barrier
; #define PG8_MMA(ai, bj, At, Bt) do { __builtin_amdgcn_s_setprio(1); _Pragma("unroll") for (int m = 0; m < 4; ++m) _Pragma("unroll") for (int n = 0; n < 2; ++n) _Pragma("unroll") for (int k = 0; k < 2; ++k) \
;         acc[ai][bj][m][n] = __builtin_amdgcn_mfma_f32_16x16x32_bf16(Bt[n][k], At[m][k], acc[ai][bj][m][n], 0, 0, 0); __builtin_amdgcn_s_setprio(0); } while (0)
; #define PG8_WAIT_V(n) asm volatile("s_waitcnt vmcnt(" #n ")" ::: "memory")
; #define PG8_TRIP_HEAD(T) const int t = (T); const bool last = (t == nt - 2); \
;             const char* a1 = cA + (size_t)(t + 1) * kstep; \
;             const char* a2 = last ? nA : cA + (size_t)(t + 2) * kstep; const char* b2 = last ? nB : cB + (size_t)(t + 2) * kstep; \
;             const char* a3 = a2 + kstep; const char* b3 = b2 + kstep; \
;             if (last && has_next) S.a_ready(nxt);
; template <class Epi, class Sched, bool ALIGN_EPI = false, bool SP2 = false>
; __device__ __forceinline__ void gemm_phase(PG8_LAS unsigned char* lds, const Gemm g, const Sched& S, const Epi& E) {
;     ...
;         if constexpr (SP2) {
;             { PG8_TRIP_HEAD(0) PG8_TRIP_SP2(asm volatile("s_waitcnt vmcnt(%0)" :: "n"(8 + Epi::NST) : "memory"), PG8_MMAZ) }
;             for (int tt = 2; tt < nt; tt += 2) { PG8_TRIP_HEAD(tt) PG8_TRIP_SP2(PG8_WAIT_V(8), PG8_MMA) }
	s_mov_b32 m0, s43
	v_lshl_add_u64 v[220:221], v[208:209], 0, s[78:79]
	ds_read_b128 v[180:183], v178 offset:49152
	ds_read_b128 v[184:187], v178 offset:50176
	ds_read_b128 v[188:191], v178 offset:51200
	ds_read_b128 v[192:195], v178 offset:52224
	ds_read_b128 v[196:199], v178 offset:53248
	ds_read_b128 v[200:203], v178 offset:54272
	ds_read_b128 v[204:207], v178 offset:55296
	ds_read_b128 v[214:217], v178 offset:56320
	global_load_lds_dwordx4 v[220:221], off
	v_lshl_add_u64 v[220:221], v[208:209], 0, s[84:85]
	s_mov_b32 m0, s44
	s_nop 0
	global_load_lds_dwordx4 v[220:221], off
	v_lshl_add_u64 v[220:221], v[208:209], 0, s[54:55]
	s_mov_b32 m0, s45
	v_lshl_add_u64 v[208:209], v[208:209], 0, s[60:61]
	global_load_lds_dwordx4 v[220:221], off
	s_mov_b32 m0, s46
	s_nop 0
	global_load_lds_dwordx4 v[208:209], off
	v_lshl_add_u64 v[208:209], v[218:219], 0, s[78:79]
	s_mov_b32 m0, s36
	s_nop 0
	global_load_lds_dwordx4 v[208:209], off
	v_lshl_add_u64 v[208:209], v[218:219], 0, s[92:93]
	s_mov_b32 m0, s37
	s_nop 0
	global_load_lds_dwordx4 v[208:209], off
	s_waitcnt vmcnt(8)
	s_waitcnt lgkmcnt(0)
	s_barrier
	v_mfma_f32_16x16x32_bf16 v[56:59], v[120:123], v[180:183], v[56:59]
	v_mfma_f32_16x16x32_bf16 v[56:59], v[132:135], v[184:187], v[56:59]
	v_mfma_f32_16x16x32_bf16 v[48:51], v[120:123], v[188:191], v[48:51]
	v_mfma_f32_16x16x32_bf16 v[48:51], v[132:135], v[192:195], v[48:51]
	v_mfma_f32_16x16x32_bf16 v[32:35], v[120:123], v[196:199], v[32:35]
	v_mfma_f32_16x16x32_bf16 v[32:35], v[132:135], v[200:203], v[32:35]
	v_mfma_f32_16x16x32_bf16 v[16:19], v[120:123], v[204:207], v[16:19]
	v_mfma_f32_16x16x32_bf16 v[16:19], v[132:135], v[214:217], v[16:19]
	v_mfma_f32_16x16x32_bf16 v[52:55], v[144:147], v[180:183], v[52:55]
	v_mfma_f32_16x16x32_bf16 v[52:55], v[148:151], v[184:187], v[52:55]
	v_mfma_f32_16x16x32_bf16 v[44:47], v[144:147], v[188:191], v[44:47]
	v_mfma_f32_16x16x32_bf16 v[44:47], v[148:151], v[192:195], v[44:47]
	v_mfma_f32_16x16x32_bf16 v[28:31], v[144:147], v[196:199], v[28:31]
	v_mfma_f32_16x16x32_bf16 v[28:31], v[148:151], v[200:203], v[28:31]
	v_mfma_f32_16x16x32_bf16 v[12:15], v[144:147], v[204:207], v[12:15]
	v_mfma_f32_16x16x32_bf16 v[12:15], v[148:151], v[214:217], v[12:15]
	v_mfma_f32_16x16x32_bf16 v[64:67], v[152:155], v[180:183], v[64:67]
	v_mfma_f32_16x16x32_bf16 v[64:67], v[156:159], v[184:187], v[64:67]
	v_mfma_f32_16x16x32_bf16 v[40:43], v[152:155], v[188:191], v[40:43]
	v_mfma_f32_16x16x32_bf16 v[40:43], v[156:159], v[192:195], v[40:43]
	v_mfma_f32_16x16x32_bf16 v[24:27], v[152:155], v[196:199], v[24:27]
	v_mfma_f32_16x16x32_bf16 v[24:27], v[156:159], v[200:203], v[24:27]
	v_mfma_f32_16x16x32_bf16 v[8:11], v[152:155], v[204:207], v[8:11]
	v_mfma_f32_16x16x32_bf16 v[8:11], v[156:159], v[214:217], v[8:11]
	v_mfma_f32_16x16x32_bf16 v[60:63], v[166:169], v[180:183], v[60:63]
	v_mfma_f32_16x16x32_bf16 v[60:63], v[170:173], v[184:187], v[60:63]
	v_mfma_f32_16x16x32_bf16 v[36:39], v[166:169], v[188:191], v[36:39]
	v_mfma_f32_16x16x32_bf16 v[36:39], v[170:173], v[192:195], v[36:39]
	v_mfma_f32_16x16x32_bf16 v[20:23], v[166:169], v[196:199], v[20:23]
	v_mfma_f32_16x16x32_bf16 v[20:23], v[170:173], v[200:203], v[20:23]
	v_mfma_f32_16x16x32_bf16 v[4:7], v[166:169], v[204:207], v[4:7]
	v_mfma_f32_16x16x32_bf16 v[4:7], v[170:173], v[214:217], v[4:7]
	s_barrier
	s_add_i32 s26, s26, 2
	s_add_u32 s10, s10, 0x100
	s_addc_u32 s11, s11, 0
	s_add_u32 s24, s24, 0x100
	s_addc_u32 s25, s25, 0
	s_cmp_gt_u32 s26, 29
	s_cbranch_scc0 .LBB0_700
	s_and_b64 vcc, exec, s[16:17]
	s_cbranch_vccz .LBB0_703
	s_barrier
